# mLSTM chunk loop: batched LDS reads (S^T tiles, o2, C-update) into spare VGPRs with counted lgkmcnt
# speedup vs baseline: 1.0038x; 1.0002x over previous
.LBB0_700:
	s_add_i32 s52, s47, -1
	s_bitcmp1_b32 s52, 0
	s_cselect_b32 s0, 0xa00, 0
	s_add_i32 s83, s0, 0
	v_mov_b32_e32 v70, s83
	ds_read_b32 v150, v70 offset:64512
	v_cndmask_b32_e64 v70, 0, 1, s[84:85]
	v_mov_b32_e32 v72, 0
	v_cmp_ne_u32_e64 s[88:89], 1, v70
	s_andn2_b64 vcc, exec, s[84:85]
	v_mov_b32_e32 v104, 0
	v_mov_b32_e32 v105, 0
	v_mov_b32_e32 v106, 0
	v_mov_b32_e32 v107, 0
	s_cbranch_vccnz .LBB0_702
	ds_read_b128 v[74:77], v191
	ds_read_b128 v[78:81], v191 offset:64
	ds_read_b128 v[202:205], v191 offset:128
	ds_read_b128 v[206:209], v191 offset:192
	s_waitcnt lgkmcnt(3)
	v_mfma_f32_16x16x32_f16 v[74:77], v[74:77], v[66:69], 0
	s_waitcnt lgkmcnt(2)
	v_mfma_f32_16x16x32_f16 v[74:77], v[78:81], v[46:49], v[74:77]
	s_waitcnt lgkmcnt(1)
	v_mfma_f32_16x16x32_f16 v[74:77], v[202:205], v[42:45], v[74:77]
	s_waitcnt lgkmcnt(0)
	v_mfma_f32_16x16x32_f16 v[104:107], v[206:209], v[38:41], v[74:77]
.LBB0_702:
	v_cndmask_b32_e64 v70, 0, 1, s[14:15]
	v_cmp_ne_u32_e64 s[80:81], 1, v70
	s_andn2_b64 vcc, exec, s[14:15]
	v_mov_b32_e32 v73, 0
	s_nop 0
	v_mov_b32_e32 v74, 0
	v_mov_b32_e32 v75, 0
	s_cbranch_vccnz .LBB0_704
	ds_read_b128 v[70:73], v191 offset:4352
	ds_read_b128 v[74:77], v191 offset:4416
	ds_read_b128 v[202:205], v191 offset:4480
	ds_read_b128 v[206:209], v191 offset:4544
	s_waitcnt lgkmcnt(3)
	v_mfma_f32_16x16x32_f16 v[70:73], v[70:73], v[66:69], 0
	s_waitcnt lgkmcnt(2)
	v_mfma_f32_16x16x32_f16 v[70:73], v[74:77], v[46:49], v[70:73]
	s_waitcnt lgkmcnt(1)
	v_mfma_f32_16x16x32_f16 v[70:73], v[202:205], v[42:45], v[70:73]
	s_waitcnt lgkmcnt(0)
	v_mfma_f32_16x16x32_f16 v[72:75], v[206:209], v[38:41], v[70:73]
.LBB0_704:
	s_nop 4
	v_cndmask_b32_e64 v70, 0, 1, s[16:17]
	v_mov_b32_e32 v92, 0
	v_cmp_ne_u32_e64 s[90:91], 1, v70
	s_andn2_b64 vcc, exec, s[16:17]
	v_mov_b32_e32 v100, 0
	v_mov_b32_e32 v101, 0
	v_mov_b32_e32 v102, 0
	v_mov_b32_e32 v103, 0
	s_cbranch_vccnz .LBB0_706
	ds_read_b128 v[76:79], v191 offset:8704
	ds_read_b128 v[80:83], v191 offset:8768
	ds_read_b128 v[202:205], v191 offset:8832
	ds_read_b128 v[206:209], v191 offset:8896
	s_waitcnt lgkmcnt(3)
	v_mfma_f32_16x16x32_f16 v[76:79], v[76:79], v[66:69], 0
	s_waitcnt lgkmcnt(2)
	v_mfma_f32_16x16x32_f16 v[76:79], v[80:83], v[46:49], v[76:79]
	s_waitcnt lgkmcnt(1)
	v_mfma_f32_16x16x32_f16 v[76:79], v[202:205], v[42:45], v[76:79]
	s_waitcnt lgkmcnt(0)
	v_mfma_f32_16x16x32_f16 v[100:103], v[206:209], v[38:41], v[76:79]
.LBB0_706:
	v_cndmask_b32_e64 v70, 0, 1, s[18:19]
	v_cmp_ne_u32_e64 s[0:1], 1, v70
	s_andn2_b64 vcc, exec, s[18:19]
	v_mov_b32_e32 v93, 0
	v_mov_b32_e32 v94, 0
	v_mov_b32_e32 v95, 0
	s_cbranch_vccnz .LBB0_708
	ds_read_b128 v[76:79], v191 offset:13056
	ds_read_b128 v[80:83], v191 offset:13120
	ds_read_b128 v[202:205], v191 offset:13184
	ds_read_b128 v[206:209], v191 offset:13248
	s_waitcnt lgkmcnt(3)
	v_mfma_f32_16x16x32_f16 v[76:79], v[76:79], v[66:69], 0
	s_waitcnt lgkmcnt(2)
	v_mfma_f32_16x16x32_f16 v[76:79], v[80:83], v[46:49], v[76:79]
	s_waitcnt lgkmcnt(1)
	v_mfma_f32_16x16x32_f16 v[76:79], v[202:205], v[42:45], v[76:79]
	s_waitcnt lgkmcnt(0)
	v_mfma_f32_16x16x32_f16 v[92:95], v[206:209], v[38:41], v[76:79]
.LBB0_708:
	v_cndmask_b32_e64 v70, 0, 1, s[20:21]
	v_mov_b32_e32 v84, 0
	v_cmp_ne_u32_e64 s[92:93], 1, v70
	s_andn2_b64 vcc, exec, s[20:21]
	v_mov_b32_e32 v96, 0
	v_mov_b32_e32 v97, 0
	v_mov_b32_e32 v98, 0
	v_mov_b32_e32 v99, 0
	s_cbranch_vccnz .LBB0_710
	ds_read_b128 v[76:79], v191 offset:17408
	ds_read_b128 v[80:83], v191 offset:17472
	ds_read_b128 v[202:205], v191 offset:17536
	ds_read_b128 v[206:209], v191 offset:17600
	s_waitcnt lgkmcnt(3)
	v_mfma_f32_16x16x32_f16 v[76:79], v[76:79], v[66:69], 0
	s_waitcnt lgkmcnt(2)
	v_mfma_f32_16x16x32_f16 v[76:79], v[80:83], v[46:49], v[76:79]
	s_waitcnt lgkmcnt(1)
	v_mfma_f32_16x16x32_f16 v[76:79], v[202:205], v[42:45], v[76:79]
	s_waitcnt lgkmcnt(0)
	v_mfma_f32_16x16x32_f16 v[96:99], v[206:209], v[38:41], v[76:79]
.LBB0_710:
	v_cndmask_b32_e64 v70, 0, 1, s[22:23]
	v_cmp_ne_u32_e64 s[2:3], 1, v70
	s_andn2_b64 vcc, exec, s[22:23]
	v_mov_b32_e32 v85, 0
	v_mov_b32_e32 v86, 0
	v_mov_b32_e32 v87, 0
	s_cbranch_vccnz .LBB0_712
	ds_read_b128 v[76:79], v191 offset:21760
	ds_read_b128 v[80:83], v191 offset:21824
	ds_read_b128 v[202:205], v191 offset:21888
	ds_read_b128 v[206:209], v191 offset:21952
	s_waitcnt lgkmcnt(3)
	v_mfma_f32_16x16x32_f16 v[76:79], v[76:79], v[66:69], 0
	s_waitcnt lgkmcnt(2)
	v_mfma_f32_16x16x32_f16 v[76:79], v[80:83], v[46:49], v[76:79]
	s_waitcnt lgkmcnt(1)
	v_mfma_f32_16x16x32_f16 v[76:79], v[202:205], v[42:45], v[76:79]
	s_waitcnt lgkmcnt(0)
	v_mfma_f32_16x16x32_f16 v[84:87], v[206:209], v[38:41], v[76:79]
.LBB0_712:
	v_cndmask_b32_e64 v70, 0, 1, s[24:25]
	s_nop 3
	v_mov_b32_e32 v78, 0
	v_cmp_ne_u32_e64 s[94:95], 1, v70
	s_andn2_b64 vcc, exec, s[24:25]
	v_mov_b32_e32 v88, 0
	v_mov_b32_e32 v89, 0
	v_mov_b32_e32 v90, 0
	v_mov_b32_e32 v91, 0
	s_cbranch_vccnz .LBB0_714
	ds_read_b128 v[80:83], v191 offset:26112
	ds_read_b128 v[88:91], v191 offset:26176
	ds_read_b128 v[202:205], v191 offset:26240
	ds_read_b128 v[206:209], v191 offset:26304
	s_waitcnt lgkmcnt(3)
	v_mfma_f32_16x16x32_f16 v[80:83], v[80:83], v[66:69], 0
	s_waitcnt lgkmcnt(2)
	v_mfma_f32_16x16x32_f16 v[80:83], v[88:91], v[46:49], v[80:83]
	s_waitcnt lgkmcnt(1)
	v_mfma_f32_16x16x32_f16 v[80:83], v[202:205], v[42:45], v[80:83]
	s_waitcnt lgkmcnt(0)
	v_mfma_f32_16x16x32_f16 v[88:91], v[206:209], v[38:41], v[80:83]
.LBB0_714:
	v_cndmask_b32_e64 v70, 0, 1, s[26:27]
	v_cmp_ne_u32_e64 s[96:97], 1, v70
	s_andn2_b64 vcc, exec, s[26:27]
	v_mov_b32_e32 v79, 0
	s_nop 0
	v_mov_b32_e32 v80, 0
	v_mov_b32_e32 v81, 0
	s_cbranch_vccnz .LBB0_716
	ds_read_b128 v[76:79], v191 offset:30464
	ds_read_b128 v[80:83], v191 offset:30528
	ds_read_b128 v[202:205], v191 offset:30592
	ds_read_b128 v[206:209], v191 offset:30656
	s_waitcnt lgkmcnt(3)
	v_mfma_f32_16x16x32_f16 v[76:79], v[76:79], v[66:69], 0
	s_waitcnt lgkmcnt(2)
	v_mfma_f32_16x16x32_f16 v[76:79], v[80:83], v[46:49], v[76:79]
	s_waitcnt lgkmcnt(1)
	v_mfma_f32_16x16x32_f16 v[76:79], v[202:205], v[42:45], v[76:79]
	s_waitcnt lgkmcnt(0)
	v_mfma_f32_16x16x32_f16 v[78:81], v[206:209], v[38:41], v[76:79]

.LBB0_763:
	ds_read_b128 v[74:77], v191 offset:49152
	ds_read_b128 v[82:85], v191 offset:53504
	ds_read_b128 v[90:93], v191 offset:57856
	ds_read_b128 v[202:205], v191 offset:49216
	ds_read_b128 v[206:209], v191 offset:53568
	ds_read_b128 v[214:217], v191 offset:57920
	ds_read_b128 v[218:221], v191 offset:49280
	ds_read_b128 v[222:225], v191 offset:53632
	ds_read_b128 v[226:229], v191 offset:57984
	ds_read_b128 v[230:233], v191 offset:49344
	ds_read_b128 v[234:237], v191 offset:53696
	ds_read_b128 v[238:241], v191 offset:58048
	s_cmp_lt_u32 s52, 2
	s_cselect_b64 vcc, -1, 0
	s_and_b64 s[0:1], vcc, exec
	s_movk_i32 s0, 0x7ff
	s_nop 0
	v_cndmask_b32_e32 v71, v157, v151, vcc
	s_cselect_b32 s0, 0xff, s0
	s_waitcnt lgkmcnt(11)
	v_mfma_f32_16x16x32_f16 v[74:77], v[74:77], v[66:69], 0
	v_add_u32_e32 v73, s48, v71
	v_sub_u32_e32 v71, s0, v71
	v_mov_b32_e32 v72, s46
	s_waitcnt lgkmcnt(10)
	v_mfma_f32_16x16x32_f16 v[82:85], v[82:85], v[66:69], 0
	v_cndmask_b32_e32 v72, v72, v195, vcc
	v_add_u32_e32 v71, s49, v71
	v_add_u32_e32 v71, 0x80, v71
	s_waitcnt lgkmcnt(9)
	v_mfma_f32_16x16x32_f16 v[66:69], v[90:93], v[66:69], 0
	v_cndmask_b32_e64 v71, v71, v73, s[86:87]
	v_add_u32_e32 v72, v71, v72
	s_waitcnt lgkmcnt(8)
	v_mfma_f32_16x16x32_f16 v[74:77], v[202:205], v[46:49], v[74:77]
	v_ashrrev_i32_e32 v73, 31, v72
	v_pk_mul_f32 v[32:33], v[32:33], v[150:151] op_sel_hi:[1,0]
	s_waitcnt lgkmcnt(7)
	v_mfma_f32_16x16x32_f16 v[82:85], v[206:209], v[46:49], v[82:85]
	v_pk_mul_f32 v[30:31], v[30:31], v[150:151] op_sel_hi:[1,0]
	v_pk_mul_f32 v[36:37], v[36:37], v[150:151] op_sel_hi:[1,0]
	s_waitcnt lgkmcnt(6)
	v_mfma_f32_16x16x32_f16 v[46:49], v[214:217], v[46:49], v[66:69]
	v_pk_mul_f32 v[34:35], v[34:35], v[150:151] op_sel_hi:[1,0]
	v_pk_mul_f32 v[28:29], v[28:29], v[150:151] op_sel_hi:[1,0]
	s_waitcnt lgkmcnt(5)
	v_mfma_f32_16x16x32_f16 v[66:69], v[218:221], v[42:45], v[74:77]
	v_pk_mul_f32 v[26:27], v[26:27], v[150:151] op_sel_hi:[1,0]
	s_waitcnt lgkmcnt(4)
	v_mfma_f32_16x16x32_f16 v[74:77], v[222:225], v[42:45], v[82:85]
	s_waitcnt lgkmcnt(3)
	v_mfma_f32_16x16x32_f16 v[42:45], v[226:229], v[42:45], v[46:49]
	s_waitcnt lgkmcnt(2)
	v_mfma_f32_16x16x32_f16 v[46:49], v[230:233], v[38:41], v[66:69]
	s_waitcnt lgkmcnt(1)
	v_mfma_f32_16x16x32_f16 v[66:69], v[234:237], v[38:41], v[74:77]
	s_waitcnt lgkmcnt(0)
	v_mfma_f32_16x16x32_f16 v[38:41], v[238:241], v[38:41], v[42:45]
	v_lshl_add_u32 v74, v116, 1, s83
	s_nop 6
	ds_read2st64_b32 v[40:41], v141 offset0:247 offset1:249
	s_waitcnt lgkmcnt(0)
	v_fmac_f32_e32 v70, v41, v38
	v_and_or_b32 v38, v184, 64, v117
	v_lshlrev_b32_e32 v38, 2, v38
	ds_bpermute_b32 v38, v38, v70
	v_max_f32_e32 v39, v40, v40
	v_mov_b32_e32 v70, v41
	v_pk_fma_f32 v[46:47], v[46:47], v[70:71], v[78:79] op_sel_hi:[1,0,1]
	s_waitcnt lgkmcnt(0)
	v_max_f32_e64 v38, |v38|, |v38|
	v_max_f32_e32 v38, v38, v39
	v_div_scale_f32 v39, s[0:1], v38, v38, 1.0
	v_rcp_f32_e32 v40, v39
	s_or_b64 s[0:1], s[6:7], s[36:37]
	v_fma_f32 v42, -v39, v40, 1.0
	v_fmac_f32_e32 v40, v42, v40
	v_div_scale_f32 v42, vcc, 1.0, v38, 1.0
	v_mul_f32_e32 v43, v42, v40
	v_fma_f32 v44, -v39, v43, v42
	v_fmac_f32_e32 v43, v44, v40
	v_fma_f32 v39, -v39, v43, v42
	v_div_fmas_f32 v39, v39, v40, v43
	v_div_fixup_f32 v42, v39, v38, 1.0
	v_lshl_add_u64 v[38:39], v[72:73], 0, s[30:31]
	v_lshlrev_b64 v[38:39], 11, v[38:39]
	v_lshl_add_u64 v[44:45], v[146:147], 0, v[38:39]
	v_pk_fma_f32 v[38:39], v[48:49], v[70:71], v[80:81] op_sel_hi:[1,0,1]
	s_and_b64 vcc, exec, s[0:1]
	v_pk_mul_f32 v[40:41], v[38:39], v[42:43] op_sel_hi:[1,0]
	v_pk_mul_f32 v[38:39], v[46:47], v[42:43] op_sel_hi:[1,0]
	global_store_dwordx4 v[44:45], v[38:41], off
	v_pk_fma_f32 v[46:47], v[66:67], v[70:71], v[86:87] op_sel_hi:[1,0,1]
	s_nop 0
	v_pk_fma_f32 v[38:39], v[68:69], v[70:71], v[88:89] op_sel_hi:[1,0,1]
	s_nop 0
	v_pk_mul_f32 v[40:41], v[38:39], v[42:43] op_sel_hi:[1,0]
	v_pk_mul_f32 v[38:39], v[46:47], v[42:43] op_sel_hi:[1,0]
	global_store_dwordx4 v[44:45], v[38:41], off offset:64
	s_nop 1
	ds_read_b64_tr_b16 v[70:71], v168 offset:0
	ds_read_b64_tr_b16 v[72:73], v168 offset:1088
	ds_read_b128 v[66:69], v74 offset:64256
	ds_read_b64_tr_b16 v[46:47], v169 offset:0
	ds_read_b64_tr_b16 v[48:49], v169 offset:448
	ds_read_b64_tr_b16 v[42:43], v169 offset:32
	ds_read_b64_tr_b16 v[44:45], v169 offset:480
	ds_read_b64_tr_b16 v[38:39], v169 offset:64
	ds_read_b64_tr_b16 v[40:41], v169 offset:512
	ds_read_b64_tr_b16 v[214:215], v171 offset:0
	ds_read_b64_tr_b16 v[216:217], v171 offset:448
	ds_read_b64_tr_b16 v[218:219], v171 offset:32
	ds_read_b64_tr_b16 v[220:221], v171 offset:480
	ds_read_b64_tr_b16 v[222:223], v171 offset:64
	ds_read_b64_tr_b16 v[224:225], v171 offset:512
	s_waitcnt lgkmcnt(6)
	v_pk_mul_f16 v69, v69, v73
	v_pk_mul_f16 v68, v68, v72
	v_pk_mul_f16 v67, v67, v71
	v_pk_mul_f16 v66, v66, v70
	s_nop 1
	v_mfma_f32_16x16x32_f16 v[30:33], v[66:69], v[46:49], v[30:33]
	v_mfma_f32_16x16x32_f16 v[34:37], v[66:69], v[42:45], v[34:37]
	v_mfma_f32_16x16x32_f16 v[26:29], v[66:69], v[38:41], v[26:29]
	ds_read_b64_tr_b16 v[230:231], v170 offset:0
	ds_read_b64_tr_b16 v[232:233], v170 offset:1088
	ds_read_b128 v[226:229], v74 offset:64320
	ds_read_b64_tr_b16 v[46:47], v173 offset:0
	ds_read_b64_tr_b16 v[48:49], v173 offset:448
	ds_read_b64_tr_b16 v[42:43], v173 offset:32
	ds_read_b64_tr_b16 v[44:45], v173 offset:480
	ds_read_b64_tr_b16 v[38:39], v173 offset:64
	ds_read_b64_tr_b16 v[40:41], v173 offset:512
	s_waitcnt lgkmcnt(6)
	v_pk_mul_f16 v229, v229, v233
	v_pk_mul_f16 v228, v228, v232
	v_pk_mul_f16 v227, v227, v231
	v_pk_mul_f16 v226, v226, v230
	s_nop 1
	v_mfma_f32_16x16x32_f16 v[30:33], v[226:229], v[214:217], v[30:33]
	v_mfma_f32_16x16x32_f16 v[34:37], v[226:229], v[218:221], v[34:37]
	v_mfma_f32_16x16x32_f16 v[26:29], v[226:229], v[222:225], v[26:29]
	ds_read_b64_tr_b16 v[70:71], v172 offset:0
	ds_read_b64_tr_b16 v[72:73], v172 offset:1088
	ds_read_b128 v[66:69], v74 offset:64384
	ds_read_b64_tr_b16 v[214:215], v175 offset:0
	ds_read_b64_tr_b16 v[216:217], v175 offset:448
	ds_read_b64_tr_b16 v[218:219], v175 offset:32
	ds_read_b64_tr_b16 v[220:221], v175 offset:480
	ds_read_b64_tr_b16 v[222:223], v175 offset:64
	ds_read_b64_tr_b16 v[224:225], v175 offset:512
	s_waitcnt lgkmcnt(6)
	v_pk_mul_f16 v69, v69, v73
	v_pk_mul_f16 v68, v68, v72
	v_pk_mul_f16 v67, v67, v71
	v_pk_mul_f16 v66, v66, v70
	s_nop 1
	v_mfma_f32_16x16x32_f16 v[30:33], v[66:69], v[46:49], v[30:33]
	v_mfma_f32_16x16x32_f16 v[34:37], v[66:69], v[42:45], v[34:37]
	v_mfma_f32_16x16x32_f16 v[26:29], v[66:69], v[38:41], v[26:29]
	ds_read_b64_tr_b16 v[230:231], v174 offset:0
	ds_read_b64_tr_b16 v[232:233], v174 offset:1088
	ds_read_b128 v[226:229], v74 offset:64448
	s_waitcnt lgkmcnt(0)
	v_pk_mul_f16 v229, v229, v233
	v_pk_mul_f16 v228, v228, v232
	v_pk_mul_f16 v227, v227, v231
	v_pk_mul_f16 v226, v226, v230
	s_nop 1
	v_mfma_f32_16x16x32_f16 v[30:33], v[226:229], v[214:217], v[30:33]
	v_mfma_f32_16x16x32_f16 v[34:37], v[226:229], v[218:221], v[34:37]
	v_mfma_f32_16x16x32_f16 v[26:29], v[226:229], v[222:225], v[26:29]
	s_cbranch_vccnz .LBB0_684
	ds_read_b32 v40, v139 offset:9216
	ds_read2st64_b32 v[38:39], v139 offset1:1
	s_waitcnt lgkmcnt(0)
	v_add_f32_e32 v41, v194, v40
	v_cmp_le_f32_e32 vcc, 0, v41
	s_and_saveexec_b64 s[0:1], vcc
	s_xor_b64 s[0:1], exec, s[0:1]
	s_cbranch_execz .LBB0_766
	v_mul_f32_e32 v40, 0xbfb8aa3b, v41
	v_exp_f32_e32 v70, v40
	s_nop 0
	v_add_f32_e32 v42, 1.0, v70
	v_frexp_mant_f32_e32 v44, v42
	v_cvt_f64_f32_e32 v[40:41], v42
	v_frexp_exp_i32_f64_e32 v40, v[40:41]
	v_cmp_gt_f32_e32 vcc, s42, v44
	v_add_f32_e32 v43, -1.0, v42
	v_sub_f32_e32 v45, v43, v42
	v_subbrev_co_u32_e32 v48, vcc, 0, v40, vcc
	v_sub_u32_e32 v40, 0, v48
	v_sub_f32_e32 v43, v70, v43
	v_add_f32_e32 v45, 1.0, v45
	v_ldexp_f32 v41, v42, v40
	v_add_f32_e32 v43, v43, v45
	v_add_f32_e32 v42, -1.0, v41
	v_add_f32_e32 v44, 1.0, v41
	v_ldexp_f32 v40, v43, v40
	v_add_f32_e32 v43, 1.0, v42
	v_add_f32_e32 v45, -1.0, v44
	v_sub_f32_e32 v43, v41, v43
	v_sub_f32_e32 v41, v41, v45
	v_add_f32_e32 v43, v40, v43
	v_add_f32_e32 v40, v40, v41
	v_add_f32_e32 v49, v44, v40
	v_rcp_f32_e32 v67, v49
	v_sub_f32_e32 v41, v49, v44
	v_sub_f32_e32 v66, v40, v41
	v_add_f32_e32 v41, v42, v43
	v_mul_f32_e32 v69, v41, v67
	v_sub_f32_e32 v40, v41, v42
	v_mul_f32_e32 v42, v49, v69
	v_fma_f32 v44, v69, v49, -v42
	v_fmac_f32_e32 v44, v69, v66
	v_sub_f32_e32 v68, v43, v40
	v_add_f32_e32 v40, v42, v44
	v_sub_f32_e32 v43, v41, v40
	v_pk_add_f32 v[46:47], v[40:41], v[42:43] neg_lo:[0,1] neg_hi:[0,1]
	v_mov_b32_e32 v45, v40
	v_pk_add_f32 v[40:41], v[46:47], v[44:45] neg_lo:[0,1] neg_hi:[0,1]
	v_cmp_neq_f32_e32 vcc, s44, v70
	v_add_f32_e32 v41, v68, v41
	v_add_f32_e32 v40, v40, v41
	v_add_f32_e32 v41, v43, v40
	v_mul_f32_e32 v68, v67, v41
	v_mul_f32_e32 v42, v49, v68
	v_fma_f32 v44, v68, v49, -v42
	v_fmac_f32_e32 v44, v68, v66
	v_sub_f32_e32 v43, v43, v41
	v_add_f32_e32 v49, v40, v43
	v_add_f32_e32 v40, v42, v44
	v_sub_f32_e32 v43, v41, v40
	v_pk_add_f32 v[46:47], v[40:41], v[42:43] neg_lo:[0,1] neg_hi:[0,1]
	v_mov_b32_e32 v45, v40
	v_pk_add_f32 v[40:41], v[46:47], v[44:45] neg_lo:[0,1] neg_hi:[0,1]
	s_nop 0
	v_add_f32_e32 v41, v49, v41
	v_add_f32_e32 v40, v40, v41
	v_add_f32_e32 v41, v69, v68
	v_add_f32_e32 v40, v43, v40
	v_sub_f32_e32 v42, v41, v69
	v_mul_f32_e32 v40, v67, v40
	v_sub_f32_e32 v42, v68, v42
	v_add_f32_e32 v42, v42, v40
	v_add_f32_e32 v44, v41, v42
	v_mul_f32_e32 v45, v44, v44
	v_fmamk_f32 v40, v45, 0x3e9b6dac, v183
	v_fmaak_f32 v141, v45, v40, 0x3f2aaada
	v_cvt_f32_i32_e32 v40, v48
	v_sub_f32_e32 v41, v44, v41
	v_sub_f32_e32 v41, v42, v41
	v_ldexp_f32 v46, v41, 1
	v_mul_f32_e32 v41, v44, v45
	v_ldexp_f32 v43, v44, 1
	v_pk_mul_f32 v[44:45], v[40:41], v[140:141]
	s_nop 0
	v_fma_f32 v42, v40, s43, -v44
	v_fmac_f32_e32 v42, 0xb102e308, v40
	v_pk_add_f32 v[40:41], v[44:45], v[42:43]
	s_nop 0
	v_sub_f32_e32 v43, v41, v43
	v_sub_f32_e32 v43, v45, v43
	v_add_f32_e32 v47, v46, v43
	v_mov_b32_e32 v46, v44
	v_pk_add_f32 v[44:45], v[40:41], v[44:45] neg_lo:[0,1] neg_hi:[0,1]
	v_pk_add_f32 v[48:49], v[40:41], v[46:47]
	v_mov_b32_e32 v43, v40
	v_mov_b32_e32 v45, v49
	v_pk_add_f32 v[66:67], v[42:43], v[44:45] neg_lo:[0,1] neg_hi:[0,1]
	v_pk_add_f32 v[42:43], v[42:43], v[44:45]
	v_mov_b32_e32 v46, v47
	v_pk_add_f32 v[44:45], v[42:43], v[40:41] op_sel:[1,0] op_sel_hi:[0,1] neg_lo:[0,1] neg_hi:[0,1]
	v_pk_add_f32 v[68:69], v[48:49], v[44:45] op_sel_hi:[1,0] neg_lo:[0,1] neg_hi:[0,1]
	v_mov_b32_e32 v48, v49
	v_mov_b32_e32 v49, v43
	v_pk_mov_b32 v[44:45], v[40:41], v[44:45] op_sel:[1,0]
	v_mov_b32_e32 v47, v40
	v_pk_add_f32 v[44:45], v[48:49], v[44:45] neg_lo:[0,1] neg_hi:[0,1]
	v_mov_b32_e32 v68, v66
	v_pk_add_f32 v[40:41], v[46:47], v[44:45] neg_lo:[0,1] neg_hi:[0,1]
	v_mov_b32_e32 v67, v43
	v_pk_add_f32 v[44:45], v[68:69], v[40:41]
	s_nop 0
	v_pk_add_f32 v[46:47], v[44:45], v[44:45] op_sel:[0,1] op_sel_hi:[1,0]
	s_nop 0
	v_pk_add_f32 v[42:43], v[42:43], v[46:47] op_sel:[1,0] op_sel_hi:[0,1]
	v_mov_b32_e32 v45, v42
	v_pk_add_f32 v[48:49], v[44:45], v[66:67] neg_lo:[0,1] neg_hi:[0,1]
	v_mov_b32_e32 v41, v46
	v_sub_f32_e32 v43, v44, v48
	v_pk_add_f32 v[40:41], v[40:41], v[48:49] neg_lo:[0,1] neg_hi:[0,1]
	v_sub_f32_e32 v43, v66, v43
	v_add_f32_e32 v40, v40, v43
	v_add_f32_e32 v40, v40, v41
	v_add_f32_e32 v40, v42, v40
	v_cndmask_b32_e32 v40, v187, v40, vcc
	v_cmp_ngt_f32_e32 vcc, -1.0, v70
	s_nop 1
	v_cndmask_b32_e32 v40, v188, v40, vcc
	v_cmp_neq_f32_e32 vcc, -1.0, v70
	s_nop 1
	v_cndmask_b32_e32 v40, v189, v40, vcc
	v_cmp_lt_f32_e64 vcc, |v70|, s45
	s_nop 1
	v_cndmask_b32_e32 v40, v40, v70, vcc
	v_xor_b32_e32 v40, 0x80000000, v40

.LBB0_2100:
	s_add_i32 s56, s52, -1
	s_bitcmp1_b32 s56, 0
	s_cselect_b32 s0, 0xa00, 0
	s_add_i32 s9, s0, 0
	v_mov_b32_e32 v70, s9
	ds_read_b32 v146, v70 offset:64512
	v_cndmask_b32_e64 v70, 0, 1, s[82:83]
	v_mov_b32_e32 v72, 0
	v_cmp_ne_u32_e64 s[88:89], 1, v70
	s_andn2_b64 vcc, exec, s[82:83]
	v_mov_b32_e32 v100, 0
	v_mov_b32_e32 v101, 0
	v_mov_b32_e32 v102, 0
	v_mov_b32_e32 v103, 0
	s_cbranch_vccnz .LBB0_2102
	ds_read_b128 v[74:77], v187
	ds_read_b128 v[78:81], v187 offset:64
	ds_read_b128 v[202:205], v187 offset:128
	ds_read_b128 v[206:209], v187 offset:192
	s_waitcnt lgkmcnt(3)
	v_mfma_f32_16x16x32_f16 v[74:77], v[74:77], v[66:69], 0
	s_waitcnt lgkmcnt(2)
	v_mfma_f32_16x16x32_f16 v[74:77], v[78:81], v[46:49], v[74:77]
	s_waitcnt lgkmcnt(1)
	v_mfma_f32_16x16x32_f16 v[74:77], v[202:205], v[42:45], v[74:77]
	s_waitcnt lgkmcnt(0)
	v_mfma_f32_16x16x32_f16 v[100:103], v[206:209], v[38:41], v[74:77]
.LBB0_2102:
	v_cndmask_b32_e64 v70, 0, 1, s[14:15]
	v_cmp_ne_u32_e64 s[80:81], 1, v70
	s_andn2_b64 vcc, exec, s[14:15]
	v_mov_b32_e32 v73, 0
	s_nop 0
	v_mov_b32_e32 v74, 0
	v_mov_b32_e32 v75, 0
	s_cbranch_vccnz .LBB0_2104
	ds_read_b128 v[70:73], v187 offset:4352
	ds_read_b128 v[74:77], v187 offset:4416
	ds_read_b128 v[202:205], v187 offset:4480
	ds_read_b128 v[206:209], v187 offset:4544
	s_waitcnt lgkmcnt(3)
	v_mfma_f32_16x16x32_f16 v[70:73], v[70:73], v[66:69], 0
	s_waitcnt lgkmcnt(2)
	v_mfma_f32_16x16x32_f16 v[70:73], v[74:77], v[46:49], v[70:73]
	s_waitcnt lgkmcnt(1)
	v_mfma_f32_16x16x32_f16 v[70:73], v[202:205], v[42:45], v[70:73]
	s_waitcnt lgkmcnt(0)
	v_mfma_f32_16x16x32_f16 v[72:75], v[206:209], v[38:41], v[70:73]
.LBB0_2104:
	s_nop 4
	v_cndmask_b32_e64 v70, 0, 1, s[16:17]
	v_mov_b32_e32 v76, 0
	v_cmp_ne_u32_e64 s[90:91], 1, v70
	s_andn2_b64 vcc, exec, s[16:17]
	v_mov_b32_e32 v96, 0
	v_mov_b32_e32 v97, 0
	v_mov_b32_e32 v98, 0
	v_mov_b32_e32 v99, 0
	s_cbranch_vccnz .LBB0_2106
	ds_read_b128 v[78:81], v187 offset:8704
	ds_read_b128 v[82:85], v187 offset:8768
	ds_read_b128 v[202:205], v187 offset:8832
	ds_read_b128 v[206:209], v187 offset:8896
	s_waitcnt lgkmcnt(3)
	v_mfma_f32_16x16x32_f16 v[78:81], v[78:81], v[66:69], 0
	s_waitcnt lgkmcnt(2)
	v_mfma_f32_16x16x32_f16 v[78:81], v[82:85], v[46:49], v[78:81]
	s_waitcnt lgkmcnt(1)
	v_mfma_f32_16x16x32_f16 v[78:81], v[202:205], v[42:45], v[78:81]
	s_waitcnt lgkmcnt(0)
	v_mfma_f32_16x16x32_f16 v[96:99], v[206:209], v[38:41], v[78:81]
.LBB0_2106:
	v_cndmask_b32_e64 v70, 0, 1, s[18:19]
	v_cmp_ne_u32_e64 s[0:1], 1, v70
	s_andn2_b64 vcc, exec, s[18:19]
	v_mov_b32_e32 v77, 0
	s_nop 0
	v_mov_b32_e32 v78, 0
	v_mov_b32_e32 v79, 0
	s_cbranch_vccnz .LBB0_2108
	ds_read_b128 v[76:79], v187 offset:13056
	ds_read_b128 v[80:83], v187 offset:13120
	ds_read_b128 v[202:205], v187 offset:13184
	ds_read_b128 v[206:209], v187 offset:13248
	s_waitcnt lgkmcnt(3)
	v_mfma_f32_16x16x32_f16 v[76:79], v[76:79], v[66:69], 0
	s_waitcnt lgkmcnt(2)
	v_mfma_f32_16x16x32_f16 v[76:79], v[80:83], v[46:49], v[76:79]
	s_waitcnt lgkmcnt(1)
	v_mfma_f32_16x16x32_f16 v[76:79], v[202:205], v[42:45], v[76:79]
	s_waitcnt lgkmcnt(0)
	v_mfma_f32_16x16x32_f16 v[76:79], v[206:209], v[38:41], v[76:79]
.LBB0_2108:
	v_cndmask_b32_e64 v70, 0, 1, s[20:21]
	v_mov_b32_e32 v80, 0
	v_cmp_ne_u32_e64 s[92:93], 1, v70
	s_andn2_b64 vcc, exec, s[20:21]
	v_mov_b32_e32 v92, 0
	v_mov_b32_e32 v93, 0
	v_mov_b32_e32 v94, 0
	v_mov_b32_e32 v95, 0
	s_cbranch_vccnz .LBB0_2110
	ds_read_b128 v[82:85], v187 offset:17408
	ds_read_b128 v[86:89], v187 offset:17472
	ds_read_b128 v[202:205], v187 offset:17536
	ds_read_b128 v[206:209], v187 offset:17600
	s_waitcnt lgkmcnt(3)
	v_mfma_f32_16x16x32_f16 v[82:85], v[82:85], v[66:69], 0
	s_waitcnt lgkmcnt(2)
	v_mfma_f32_16x16x32_f16 v[82:85], v[86:89], v[46:49], v[82:85]
	s_waitcnt lgkmcnt(1)
	v_mfma_f32_16x16x32_f16 v[82:85], v[202:205], v[42:45], v[82:85]
	s_waitcnt lgkmcnt(0)
	v_mfma_f32_16x16x32_f16 v[92:95], v[206:209], v[38:41], v[82:85]
.LBB0_2110:
	v_cndmask_b32_e64 v70, 0, 1, s[22:23]
	v_cmp_ne_u32_e64 s[2:3], 1, v70
	s_andn2_b64 vcc, exec, s[22:23]
	v_mov_b32_e32 v81, 0
	s_nop 0
	v_mov_b32_e32 v82, 0
	v_mov_b32_e32 v83, 0
	s_cbranch_vccnz .LBB0_2112
	ds_read_b128 v[80:83], v187 offset:21760
	ds_read_b128 v[84:87], v187 offset:21824
	ds_read_b128 v[202:205], v187 offset:21888
	ds_read_b128 v[206:209], v187 offset:21952
	s_waitcnt lgkmcnt(3)
	v_mfma_f32_16x16x32_f16 v[80:83], v[80:83], v[66:69], 0
	s_waitcnt lgkmcnt(2)
	v_mfma_f32_16x16x32_f16 v[80:83], v[84:87], v[46:49], v[80:83]
	s_waitcnt lgkmcnt(1)
	v_mfma_f32_16x16x32_f16 v[80:83], v[202:205], v[42:45], v[80:83]
	s_waitcnt lgkmcnt(0)
	v_mfma_f32_16x16x32_f16 v[80:83], v[206:209], v[38:41], v[80:83]
.LBB0_2112:
	v_cndmask_b32_e64 v70, 0, 1, s[24:25]
	v_mov_b32_e32 v84, 0
	v_cmp_ne_u32_e64 s[94:95], 1, v70
	s_andn2_b64 vcc, exec, s[24:25]
	v_mov_b32_e32 v88, 0
	v_mov_b32_e32 v89, 0
	v_mov_b32_e32 v90, 0
	v_mov_b32_e32 v91, 0
	s_cbranch_vccnz .LBB0_2114
	ds_read_b128 v[86:89], v187 offset:26112
	ds_read_b128 v[192:195], v187 offset:26176
	ds_read_b128 v[202:205], v187 offset:26240
	ds_read_b128 v[206:209], v187 offset:26304
	s_waitcnt lgkmcnt(3)
	v_mfma_f32_16x16x32_f16 v[86:89], v[86:89], v[66:69], 0
	s_waitcnt lgkmcnt(2)
	v_mfma_f32_16x16x32_f16 v[86:89], v[192:195], v[46:49], v[86:89]
	s_waitcnt lgkmcnt(1)
	v_mfma_f32_16x16x32_f16 v[86:89], v[202:205], v[42:45], v[86:89]
	s_waitcnt lgkmcnt(0)
	v_mfma_f32_16x16x32_f16 v[88:91], v[206:209], v[38:41], v[86:89]
.LBB0_2114:
	v_cndmask_b32_e64 v70, 0, 1, s[26:27]
	v_cmp_ne_u32_e64 s[96:97], 1, v70
	s_andn2_b64 vcc, exec, s[26:27]
	v_mov_b32_e32 v85, 0
	s_nop 0
	v_mov_b32_e32 v86, 0
	v_mov_b32_e32 v87, 0
	s_cbranch_vccnz .LBB0_2116
	ds_read_b128 v[84:87], v187 offset:30464
	ds_read_b128 v[192:195], v187 offset:30528
	ds_read_b128 v[202:205], v187 offset:30592
	ds_read_b128 v[206:209], v187 offset:30656
	s_waitcnt lgkmcnt(3)
	v_mfma_f32_16x16x32_f16 v[84:87], v[84:87], v[66:69], 0
	s_waitcnt lgkmcnt(2)
	v_mfma_f32_16x16x32_f16 v[84:87], v[192:195], v[46:49], v[84:87]
	s_waitcnt lgkmcnt(1)
	v_mfma_f32_16x16x32_f16 v[84:87], v[202:205], v[42:45], v[84:87]
	s_waitcnt lgkmcnt(0)
	v_mfma_f32_16x16x32_f16 v[84:87], v[206:209], v[38:41], v[84:87]

.LBB0_2175:
	ds_read_b128 v[74:77], v187 offset:49152
	ds_read_b128 v[78:81], v187 offset:53504
	ds_read_b128 v[82:85], v187 offset:57856
	ds_read_b128 v[202:205], v187 offset:49216
	ds_read_b128 v[206:209], v187 offset:53568
	ds_read_b128 v[214:217], v187 offset:57920
	ds_read_b128 v[218:221], v187 offset:49280
	ds_read_b128 v[222:225], v187 offset:53632
	ds_read_b128 v[226:229], v187 offset:57984
	ds_read_b128 v[230:233], v187 offset:49344
	ds_read_b128 v[234:237], v187 offset:53696
	ds_read_b128 v[238:241], v187 offset:58048
	s_cmp_lt_u32 s56, 2
	s_cselect_b64 vcc, -1, 0
	s_and_b64 s[0:1], vcc, exec
	s_movk_i32 s0, 0x7ff
	s_nop 0
	v_cndmask_b32_e32 v71, v153, v147, vcc
	s_cselect_b32 s0, 0xff, s0
	s_waitcnt lgkmcnt(11)
	v_mfma_f32_16x16x32_f16 v[74:77], v[74:77], v[66:69], 0
	v_add_u32_e32 v73, s55, v71
	v_sub_u32_e32 v71, s0, v71
	v_mov_b32_e32 v72, s51
	s_waitcnt lgkmcnt(10)
	v_mfma_f32_16x16x32_f16 v[78:81], v[78:81], v[66:69], 0
	v_cndmask_b32_e32 v72, v72, v191, vcc
	v_add_u32_e32 v71, s53, v71
	v_cndmask_b32_e64 v71, v71, v73, s[86:87]
	s_waitcnt lgkmcnt(9)
	v_mfma_f32_16x16x32_f16 v[66:69], v[82:85], v[66:69], 0
	v_add_u32_e32 v72, v71, v72
	v_ashrrev_i32_e32 v73, 31, v72
	s_waitcnt lgkmcnt(8)
	v_mfma_f32_16x16x32_f16 v[74:77], v[202:205], v[46:49], v[74:77]
	v_pk_mul_f32 v[32:33], v[32:33], v[146:147] op_sel_hi:[1,0]
	v_pk_mul_f32 v[30:31], v[30:31], v[146:147] op_sel_hi:[1,0]
	s_waitcnt lgkmcnt(7)
	v_mfma_f32_16x16x32_f16 v[78:81], v[206:209], v[46:49], v[78:81]
	v_pk_mul_f32 v[36:37], v[36:37], v[146:147] op_sel_hi:[1,0]
	v_pk_mul_f32 v[34:35], v[34:35], v[146:147] op_sel_hi:[1,0]
	s_waitcnt lgkmcnt(6)
	v_mfma_f32_16x16x32_f16 v[46:49], v[214:217], v[46:49], v[66:69]
	v_pk_mul_f32 v[28:29], v[28:29], v[146:147] op_sel_hi:[1,0]
	v_pk_mul_f32 v[26:27], v[26:27], v[146:147] op_sel_hi:[1,0]
	s_waitcnt lgkmcnt(5)
	v_mfma_f32_16x16x32_f16 v[66:69], v[218:221], v[42:45], v[74:77]
	s_waitcnt lgkmcnt(4)
	v_mfma_f32_16x16x32_f16 v[74:77], v[222:225], v[42:45], v[78:81]
	s_waitcnt lgkmcnt(3)
	v_mfma_f32_16x16x32_f16 v[42:45], v[226:229], v[42:45], v[46:49]
	s_waitcnt lgkmcnt(2)
	v_mfma_f32_16x16x32_f16 v[46:49], v[230:233], v[38:41], v[66:69]
	s_waitcnt lgkmcnt(1)
	v_mfma_f32_16x16x32_f16 v[66:69], v[234:237], v[38:41], v[74:77]
	s_waitcnt lgkmcnt(0)
	v_mfma_f32_16x16x32_f16 v[38:41], v[238:241], v[38:41], v[42:45]
	v_lshl_add_u32 v74, v112, 1, s9
	s_nop 6
	ds_read2st64_b32 v[40:41], v137 offset0:247 offset1:249
	s_waitcnt lgkmcnt(0)
	v_fmac_f32_e32 v70, v41, v38
	v_and_or_b32 v38, v180, 64, v113
	v_lshlrev_b32_e32 v38, 2, v38
	ds_bpermute_b32 v38, v38, v70
	v_max_f32_e32 v39, v40, v40
	v_mov_b32_e32 v70, v41
	v_pk_fma_f32 v[46:47], v[46:47], v[70:71], v[86:87] op_sel_hi:[1,0,1]
	s_waitcnt lgkmcnt(0)
	v_max_f32_e64 v38, |v38|, |v38|
	v_max_f32_e32 v38, v38, v39
	v_div_scale_f32 v39, s[0:1], v38, v38, 1.0
	v_rcp_f32_e32 v40, v39
	s_or_b64 s[0:1], s[6:7], s[36:37]
	v_fma_f32 v42, -v39, v40, 1.0
	v_fmac_f32_e32 v40, v42, v40
	v_div_scale_f32 v42, vcc, 1.0, v38, 1.0
	v_mul_f32_e32 v43, v42, v40
	v_fma_f32 v44, -v39, v43, v42
	v_fmac_f32_e32 v43, v44, v40
	v_fma_f32 v39, -v39, v43, v42
	v_div_fmas_f32 v39, v39, v40, v43
	v_div_fixup_f32 v42, v39, v38, 1.0
	v_lshl_add_u64 v[38:39], v[72:73], 0, s[34:35]
	v_lshlrev_b64 v[38:39], 11, v[38:39]
	v_lshl_add_u64 v[44:45], v[142:143], 0, v[38:39]
	v_pk_fma_f32 v[38:39], v[48:49], v[70:71], v[88:89] op_sel_hi:[1,0,1]
	s_and_b64 vcc, exec, s[0:1]
	v_pk_mul_f32 v[40:41], v[38:39], v[42:43] op_sel_hi:[1,0]
	v_pk_mul_f32 v[38:39], v[46:47], v[42:43] op_sel_hi:[1,0]
	global_store_dwordx4 v[44:45], v[38:41], off
	v_pk_fma_f32 v[46:47], v[66:67], v[70:71], v[90:91] op_sel_hi:[1,0,1]
	s_nop 0
	v_pk_fma_f32 v[38:39], v[68:69], v[70:71], v[92:93] op_sel_hi:[1,0,1]
	s_nop 0
	v_pk_mul_f32 v[40:41], v[38:39], v[42:43] op_sel_hi:[1,0]
	v_pk_mul_f32 v[38:39], v[46:47], v[42:43] op_sel_hi:[1,0]
	global_store_dwordx4 v[44:45], v[38:41], off offset:64
	s_nop 1
	ds_read_b64_tr_b16 v[70:71], v164 offset:0
	ds_read_b64_tr_b16 v[72:73], v164 offset:1088
	ds_read_b128 v[66:69], v74 offset:64256
	ds_read_b64_tr_b16 v[46:47], v165 offset:0
	ds_read_b64_tr_b16 v[48:49], v165 offset:448
	ds_read_b64_tr_b16 v[42:43], v165 offset:32
	ds_read_b64_tr_b16 v[44:45], v165 offset:480
	ds_read_b64_tr_b16 v[38:39], v165 offset:64
	ds_read_b64_tr_b16 v[40:41], v165 offset:512
	ds_read_b64_tr_b16 v[214:215], v167 offset:0
	ds_read_b64_tr_b16 v[216:217], v167 offset:448
	ds_read_b64_tr_b16 v[218:219], v167 offset:32
	ds_read_b64_tr_b16 v[220:221], v167 offset:480
	ds_read_b64_tr_b16 v[222:223], v167 offset:64
	ds_read_b64_tr_b16 v[224:225], v167 offset:512
	s_waitcnt lgkmcnt(6)
	v_pk_mul_f16 v69, v69, v73
	v_pk_mul_f16 v68, v68, v72
	v_pk_mul_f16 v67, v67, v71
	v_pk_mul_f16 v66, v66, v70
	s_nop 1
	v_mfma_f32_16x16x32_f16 v[30:33], v[66:69], v[46:49], v[30:33]
	v_mfma_f32_16x16x32_f16 v[34:37], v[66:69], v[42:45], v[34:37]
	v_mfma_f32_16x16x32_f16 v[26:29], v[66:69], v[38:41], v[26:29]
	ds_read_b64_tr_b16 v[230:231], v166 offset:0
	ds_read_b64_tr_b16 v[232:233], v166 offset:1088
	ds_read_b128 v[226:229], v74 offset:64320
	ds_read_b64_tr_b16 v[46:47], v169 offset:0
	ds_read_b64_tr_b16 v[48:49], v169 offset:448
	ds_read_b64_tr_b16 v[42:43], v169 offset:32
	ds_read_b64_tr_b16 v[44:45], v169 offset:480
	ds_read_b64_tr_b16 v[38:39], v169 offset:64
	ds_read_b64_tr_b16 v[40:41], v169 offset:512
	s_waitcnt lgkmcnt(6)
	v_pk_mul_f16 v229, v229, v233
	v_pk_mul_f16 v228, v228, v232
	v_pk_mul_f16 v227, v227, v231
	v_pk_mul_f16 v226, v226, v230
	s_nop 1
	v_mfma_f32_16x16x32_f16 v[30:33], v[226:229], v[214:217], v[30:33]
	v_mfma_f32_16x16x32_f16 v[34:37], v[226:229], v[218:221], v[34:37]
	v_mfma_f32_16x16x32_f16 v[26:29], v[226:229], v[222:225], v[26:29]
	ds_read_b64_tr_b16 v[70:71], v168 offset:0
	ds_read_b64_tr_b16 v[72:73], v168 offset:1088
	ds_read_b128 v[66:69], v74 offset:64384
	ds_read_b64_tr_b16 v[214:215], v171 offset:0
	ds_read_b64_tr_b16 v[216:217], v171 offset:448
	ds_read_b64_tr_b16 v[218:219], v171 offset:32
	ds_read_b64_tr_b16 v[220:221], v171 offset:480
	ds_read_b64_tr_b16 v[222:223], v171 offset:64
	ds_read_b64_tr_b16 v[224:225], v171 offset:512
	s_waitcnt lgkmcnt(6)
	v_pk_mul_f16 v69, v69, v73
	v_pk_mul_f16 v68, v68, v72
	v_pk_mul_f16 v67, v67, v71
	v_pk_mul_f16 v66, v66, v70
	s_nop 1
	v_mfma_f32_16x16x32_f16 v[30:33], v[66:69], v[46:49], v[30:33]
	v_mfma_f32_16x16x32_f16 v[34:37], v[66:69], v[42:45], v[34:37]
	v_mfma_f32_16x16x32_f16 v[26:29], v[66:69], v[38:41], v[26:29]
	ds_read_b64_tr_b16 v[230:231], v170 offset:0
	ds_read_b64_tr_b16 v[232:233], v170 offset:1088
	ds_read_b128 v[226:229], v74 offset:64448
	s_waitcnt lgkmcnt(0)
	v_pk_mul_f16 v229, v229, v233
	v_pk_mul_f16 v228, v228, v232
	v_pk_mul_f16 v227, v227, v231
	v_pk_mul_f16 v226, v226, v230
	s_nop 1
	v_mfma_f32_16x16x32_f16 v[30:33], v[226:229], v[214:217], v[30:33]
	v_mfma_f32_16x16x32_f16 v[34:37], v[226:229], v[218:221], v[34:37]
	v_mfma_f32_16x16x32_f16 v[26:29], v[226:229], v[222:225], v[26:29]
	s_cbranch_vccnz .LBB0_2084
	ds_read_b32 v40, v135 offset:9216
	ds_read2st64_b32 v[38:39], v135 offset1:1
	s_waitcnt lgkmcnt(0)
	v_add_f32_e32 v41, v190, v40
	v_cmp_le_f32_e32 vcc, 0, v41
	s_and_saveexec_b64 s[0:1], vcc
	s_xor_b64 s[0:1], exec, s[0:1]
	s_cbranch_execz .LBB0_2178
	v_mul_f32_e32 v40, 0xbfb8aa3b, v41
	v_exp_f32_e32 v70, v40
	s_nop 0
	v_add_f32_e32 v42, 1.0, v70
	v_frexp_mant_f32_e32 v44, v42
	v_cvt_f64_f32_e32 v[40:41], v42
	v_frexp_exp_i32_f64_e32 v40, v[40:41]
	v_cmp_gt_f32_e32 vcc, s47, v44
	v_add_f32_e32 v43, -1.0, v42
	v_sub_f32_e32 v45, v43, v42
	v_subbrev_co_u32_e32 v48, vcc, 0, v40, vcc
	v_sub_u32_e32 v40, 0, v48
	v_sub_f32_e32 v43, v70, v43
	v_add_f32_e32 v45, 1.0, v45
	v_ldexp_f32 v41, v42, v40
	v_add_f32_e32 v43, v43, v45
	v_add_f32_e32 v42, -1.0, v41
	v_add_f32_e32 v44, 1.0, v41
	v_ldexp_f32 v40, v43, v40
	v_add_f32_e32 v43, 1.0, v42
	v_add_f32_e32 v45, -1.0, v44
	v_sub_f32_e32 v43, v41, v43
	v_sub_f32_e32 v41, v41, v45
	v_add_f32_e32 v43, v40, v43
	v_add_f32_e32 v40, v40, v41
	v_add_f32_e32 v49, v44, v40
	v_rcp_f32_e32 v67, v49
	v_sub_f32_e32 v41, v49, v44
	v_sub_f32_e32 v66, v40, v41
	v_add_f32_e32 v41, v42, v43
	v_mul_f32_e32 v69, v41, v67
	v_sub_f32_e32 v40, v41, v42
	v_mul_f32_e32 v42, v49, v69
	v_fma_f32 v44, v69, v49, -v42
	v_fmac_f32_e32 v44, v69, v66
	v_sub_f32_e32 v68, v43, v40
	v_add_f32_e32 v40, v42, v44
	v_sub_f32_e32 v43, v41, v40
	v_pk_add_f32 v[46:47], v[40:41], v[42:43] neg_lo:[0,1] neg_hi:[0,1]
	v_mov_b32_e32 v45, v40
	v_pk_add_f32 v[40:41], v[46:47], v[44:45] neg_lo:[0,1] neg_hi:[0,1]
	v_cmp_neq_f32_e32 vcc, s49, v70
	v_add_f32_e32 v41, v68, v41
	v_add_f32_e32 v40, v40, v41
	v_add_f32_e32 v41, v43, v40
	v_mul_f32_e32 v68, v67, v41
	v_mul_f32_e32 v42, v49, v68
	v_fma_f32 v44, v68, v49, -v42
	v_fmac_f32_e32 v44, v68, v66
	v_sub_f32_e32 v43, v43, v41
	v_add_f32_e32 v49, v40, v43
	v_add_f32_e32 v40, v42, v44
	v_sub_f32_e32 v43, v41, v40
	v_pk_add_f32 v[46:47], v[40:41], v[42:43] neg_lo:[0,1] neg_hi:[0,1]
	v_mov_b32_e32 v45, v40
	v_pk_add_f32 v[40:41], v[46:47], v[44:45] neg_lo:[0,1] neg_hi:[0,1]
	s_nop 0
	v_add_f32_e32 v41, v49, v41
	v_add_f32_e32 v40, v40, v41
	v_add_f32_e32 v41, v69, v68
	v_add_f32_e32 v40, v43, v40
	v_sub_f32_e32 v42, v41, v69
	v_mul_f32_e32 v40, v67, v40
	v_sub_f32_e32 v42, v68, v42
	v_add_f32_e32 v42, v42, v40
	v_add_f32_e32 v44, v41, v42
	v_mul_f32_e32 v45, v44, v44
	v_fmamk_f32 v40, v45, 0x3e9b6dac, v179
	v_fmaak_f32 v137, v45, v40, 0x3f2aaada
	v_cvt_f32_i32_e32 v40, v48
	v_sub_f32_e32 v41, v44, v41
	v_sub_f32_e32 v41, v42, v41
	v_ldexp_f32 v46, v41, 1
	v_mul_f32_e32 v41, v44, v45
	v_ldexp_f32 v43, v44, 1
	v_pk_mul_f32 v[44:45], v[40:41], v[136:137]
	s_nop 0
	v_fma_f32 v42, v40, s48, -v44
	v_fmac_f32_e32 v42, 0xb102e308, v40
	v_pk_add_f32 v[40:41], v[44:45], v[42:43]
	s_nop 0
	v_sub_f32_e32 v43, v41, v43
	v_sub_f32_e32 v43, v45, v43
	v_add_f32_e32 v47, v46, v43
	v_mov_b32_e32 v46, v44
	v_pk_add_f32 v[44:45], v[40:41], v[44:45] neg_lo:[0,1] neg_hi:[0,1]
	v_pk_add_f32 v[48:49], v[40:41], v[46:47]
	v_mov_b32_e32 v43, v40
	v_mov_b32_e32 v45, v49
	v_pk_add_f32 v[66:67], v[42:43], v[44:45] neg_lo:[0,1] neg_hi:[0,1]
	v_pk_add_f32 v[42:43], v[42:43], v[44:45]
	v_mov_b32_e32 v46, v47
	v_pk_add_f32 v[44:45], v[42:43], v[40:41] op_sel:[1,0] op_sel_hi:[0,1] neg_lo:[0,1] neg_hi:[0,1]
	v_pk_add_f32 v[68:69], v[48:49], v[44:45] op_sel_hi:[1,0] neg_lo:[0,1] neg_hi:[0,1]
	v_mov_b32_e32 v48, v49
	v_mov_b32_e32 v49, v43
	v_pk_mov_b32 v[44:45], v[40:41], v[44:45] op_sel:[1,0]
	v_mov_b32_e32 v47, v40
	v_pk_add_f32 v[44:45], v[48:49], v[44:45] neg_lo:[0,1] neg_hi:[0,1]
	v_mov_b32_e32 v68, v66
	v_pk_add_f32 v[40:41], v[46:47], v[44:45] neg_lo:[0,1] neg_hi:[0,1]
	v_mov_b32_e32 v67, v43
	v_pk_add_f32 v[44:45], v[68:69], v[40:41]
	s_nop 0
	v_pk_add_f32 v[46:47], v[44:45], v[44:45] op_sel:[0,1] op_sel_hi:[1,0]
	s_nop 0
	v_pk_add_f32 v[42:43], v[42:43], v[46:47] op_sel:[1,0] op_sel_hi:[0,1]
	v_mov_b32_e32 v45, v42
	v_pk_add_f32 v[48:49], v[44:45], v[66:67] neg_lo:[0,1] neg_hi:[0,1]
	v_mov_b32_e32 v41, v46
	v_sub_f32_e32 v43, v44, v48
	v_pk_add_f32 v[40:41], v[40:41], v[48:49] neg_lo:[0,1] neg_hi:[0,1]
	v_sub_f32_e32 v43, v66, v43
	v_add_f32_e32 v40, v40, v43
	v_add_f32_e32 v40, v40, v41
	v_add_f32_e32 v40, v42, v40
	v_cndmask_b32_e32 v40, v183, v40, vcc
	v_cmp_ngt_f32_e32 vcc, -1.0, v70
	s_nop 1
	v_cndmask_b32_e32 v40, v184, v40, vcc
	v_cmp_neq_f32_e32 vcc, -1.0, v70
	s_nop 1
	v_cndmask_b32_e32 v40, v185, v40, vcc
	v_cmp_lt_f32_e64 vcc, |v70|, s50
	s_nop 1
	v_cndmask_b32_e32 v40, v40, v70, vcc
	v_xor_b32_e32 v40, 0x80000000, v40

.LBB0_3717:
	s_add_i32 s54, s49, -1
	s_bitcmp1_b32 s54, 0
	s_cselect_b32 s0, 0xa00, 0
	s_add_i32 s83, s0, 0
	v_mov_b32_e32 v70, s83
	ds_read_b32 v146, v70 offset:64512
	v_cndmask_b32_e64 v70, 0, 1, s[84:85]
	v_mov_b32_e32 v72, 0
	v_cmp_ne_u32_e64 s[88:89], 1, v70
	s_andn2_b64 vcc, exec, s[84:85]
	v_mov_b32_e32 v100, 0
	v_mov_b32_e32 v101, 0
	v_mov_b32_e32 v102, 0
	v_mov_b32_e32 v103, 0
	s_cbranch_vccnz .LBB0_3719
	ds_read_b128 v[74:77], v187
	ds_read_b128 v[78:81], v187 offset:64
	ds_read_b128 v[202:205], v187 offset:128
	ds_read_b128 v[206:209], v187 offset:192
	s_waitcnt lgkmcnt(3)
	v_mfma_f32_16x16x32_f16 v[74:77], v[74:77], v[66:69], 0
	s_waitcnt lgkmcnt(2)
	v_mfma_f32_16x16x32_f16 v[74:77], v[78:81], v[46:49], v[74:77]
	s_waitcnt lgkmcnt(1)
	v_mfma_f32_16x16x32_f16 v[74:77], v[202:205], v[42:45], v[74:77]
	s_waitcnt lgkmcnt(0)
	v_mfma_f32_16x16x32_f16 v[100:103], v[206:209], v[38:41], v[74:77]
.LBB0_3719:
	v_cndmask_b32_e64 v70, 0, 1, s[14:15]
	v_cmp_ne_u32_e64 s[0:1], 1, v70
	s_andn2_b64 vcc, exec, s[14:15]
	v_mov_b32_e32 v73, 0
	s_nop 0
	v_mov_b32_e32 v74, 0
	v_mov_b32_e32 v75, 0
	s_cbranch_vccnz .LBB0_3721
	ds_read_b128 v[70:73], v187 offset:4352
	ds_read_b128 v[74:77], v187 offset:4416
	ds_read_b128 v[202:205], v187 offset:4480
	ds_read_b128 v[206:209], v187 offset:4544
	s_waitcnt lgkmcnt(3)
	v_mfma_f32_16x16x32_f16 v[70:73], v[70:73], v[66:69], 0
	s_waitcnt lgkmcnt(2)
	v_mfma_f32_16x16x32_f16 v[70:73], v[74:77], v[46:49], v[70:73]
	s_waitcnt lgkmcnt(1)
	v_mfma_f32_16x16x32_f16 v[70:73], v[202:205], v[42:45], v[70:73]
	s_waitcnt lgkmcnt(0)
	v_mfma_f32_16x16x32_f16 v[72:75], v[206:209], v[38:41], v[70:73]

.LBB0_3723:
	v_cndmask_b32_e64 v70, 0, 1, s[18:19]
	v_cmp_ne_u32_e64 s[80:81], 1, v70
	s_andn2_b64 vcc, exec, s[18:19]
	v_mov_b32_e32 v77, 0
	s_nop 0
	v_mov_b32_e32 v78, 0
	v_mov_b32_e32 v79, 0
	s_cbranch_vccnz .LBB0_3725
	ds_read_b128 v[76:79], v187 offset:13056
	ds_read_b128 v[80:83], v187 offset:13120
	ds_read_b128 v[202:205], v187 offset:13184
	ds_read_b128 v[206:209], v187 offset:13248
	s_waitcnt lgkmcnt(3)
	v_mfma_f32_16x16x32_f16 v[76:79], v[76:79], v[66:69], 0
	s_waitcnt lgkmcnt(2)
	v_mfma_f32_16x16x32_f16 v[76:79], v[80:83], v[46:49], v[76:79]
	s_waitcnt lgkmcnt(1)
	v_mfma_f32_16x16x32_f16 v[76:79], v[202:205], v[42:45], v[76:79]
	s_waitcnt lgkmcnt(0)
	v_mfma_f32_16x16x32_f16 v[76:79], v[206:209], v[38:41], v[76:79]

.LBB0_3792:
	ds_read_b128 v[74:77], v187 offset:49152
	ds_read_b128 v[78:81], v187 offset:53504
	ds_read_b128 v[82:85], v187 offset:57856
	ds_read_b128 v[202:205], v187 offset:49216
	ds_read_b128 v[206:209], v187 offset:53568
	ds_read_b128 v[214:217], v187 offset:57920
	ds_read_b128 v[218:221], v187 offset:49280
	ds_read_b128 v[222:225], v187 offset:53632
	ds_read_b128 v[226:229], v187 offset:57984
	ds_read_b128 v[230:233], v187 offset:49344
	ds_read_b128 v[234:237], v187 offset:53696
	ds_read_b128 v[238:241], v187 offset:58048
	s_cmp_lt_u32 s54, 2
	s_cselect_b64 vcc, -1, 0
	s_and_b64 s[0:1], vcc, exec
	s_movk_i32 s0, 0x7ff
	s_nop 0
	v_cndmask_b32_e32 v71, v153, v147, vcc
	s_cselect_b32 s0, 0xff, s0
	s_waitcnt lgkmcnt(11)
	v_mfma_f32_16x16x32_f16 v[74:77], v[74:77], v[66:69], 0
	v_add_u32_e32 v73, s50, v71
	v_sub_u32_e32 v71, s0, v71
	v_mov_b32_e32 v72, s48
	s_waitcnt lgkmcnt(10)
	v_mfma_f32_16x16x32_f16 v[78:81], v[78:81], v[66:69], 0
	v_cndmask_b32_e32 v72, v72, v191, vcc
	v_add_u32_e32 v71, s51, v71
	v_add_u32_e32 v71, 0x80, v71
	s_waitcnt lgkmcnt(9)
	v_mfma_f32_16x16x32_f16 v[66:69], v[82:85], v[66:69], 0
	v_cndmask_b32_e64 v71, v71, v73, s[86:87]
	v_add_u32_e32 v72, v71, v72
	s_waitcnt lgkmcnt(8)
	v_mfma_f32_16x16x32_f16 v[74:77], v[202:205], v[46:49], v[74:77]
	v_ashrrev_i32_e32 v73, 31, v72
	v_pk_mul_f32 v[32:33], v[32:33], v[146:147] op_sel_hi:[1,0]
	s_waitcnt lgkmcnt(7)
	v_mfma_f32_16x16x32_f16 v[78:81], v[206:209], v[46:49], v[78:81]
	v_pk_mul_f32 v[30:31], v[30:31], v[146:147] op_sel_hi:[1,0]
	v_pk_mul_f32 v[36:37], v[36:37], v[146:147] op_sel_hi:[1,0]
	s_waitcnt lgkmcnt(6)
	v_mfma_f32_16x16x32_f16 v[46:49], v[214:217], v[46:49], v[66:69]
	v_pk_mul_f32 v[34:35], v[34:35], v[146:147] op_sel_hi:[1,0]
	v_pk_mul_f32 v[28:29], v[28:29], v[146:147] op_sel_hi:[1,0]
	s_waitcnt lgkmcnt(5)
	v_mfma_f32_16x16x32_f16 v[66:69], v[218:221], v[42:45], v[74:77]
	v_pk_mul_f32 v[26:27], v[26:27], v[146:147] op_sel_hi:[1,0]
	s_waitcnt lgkmcnt(4)
	v_mfma_f32_16x16x32_f16 v[74:77], v[222:225], v[42:45], v[78:81]
	s_waitcnt lgkmcnt(3)
	v_mfma_f32_16x16x32_f16 v[42:45], v[226:229], v[42:45], v[46:49]
	s_waitcnt lgkmcnt(2)
	v_mfma_f32_16x16x32_f16 v[46:49], v[230:233], v[38:41], v[66:69]
	s_waitcnt lgkmcnt(1)
	v_mfma_f32_16x16x32_f16 v[66:69], v[234:237], v[38:41], v[74:77]
	s_waitcnt lgkmcnt(0)
	v_mfma_f32_16x16x32_f16 v[38:41], v[238:241], v[38:41], v[42:45]
	v_lshl_add_u32 v74, v112, 1, s83
	s_nop 6
	ds_read2st64_b32 v[40:41], v137 offset0:247 offset1:249
	s_waitcnt lgkmcnt(0)
	v_fmac_f32_e32 v70, v41, v38
	v_and_or_b32 v38, v180, 64, v113
	v_lshlrev_b32_e32 v38, 2, v38
	ds_bpermute_b32 v38, v38, v70
	v_max_f32_e32 v39, v40, v40
	v_mov_b32_e32 v70, v41
	v_pk_fma_f32 v[46:47], v[46:47], v[70:71], v[86:87] op_sel_hi:[1,0,1]
	s_waitcnt lgkmcnt(0)
	v_max_f32_e64 v38, |v38|, |v38|
	v_max_f32_e32 v38, v38, v39
	v_div_scale_f32 v39, s[0:1], v38, v38, 1.0
	v_rcp_f32_e32 v40, v39
	s_or_b64 s[0:1], s[6:7], s[36:37]
	v_fma_f32 v42, -v39, v40, 1.0
	v_fmac_f32_e32 v40, v42, v40
	v_div_scale_f32 v42, vcc, 1.0, v38, 1.0
	v_mul_f32_e32 v43, v42, v40
	v_fma_f32 v44, -v39, v43, v42
	v_fmac_f32_e32 v43, v44, v40
	v_fma_f32 v39, -v39, v43, v42
	v_div_fmas_f32 v39, v39, v40, v43
	v_div_fixup_f32 v42, v39, v38, 1.0
	v_lshl_add_u64 v[38:39], v[72:73], 0, s[30:31]
	v_lshlrev_b64 v[38:39], 11, v[38:39]
	v_lshl_add_u64 v[44:45], v[142:143], 0, v[38:39]
	v_pk_fma_f32 v[38:39], v[48:49], v[70:71], v[88:89] op_sel_hi:[1,0,1]
	s_and_b64 vcc, exec, s[0:1]
	v_pk_mul_f32 v[40:41], v[38:39], v[42:43] op_sel_hi:[1,0]
	v_pk_mul_f32 v[38:39], v[46:47], v[42:43] op_sel_hi:[1,0]
	global_store_dwordx4 v[44:45], v[38:41], off
	v_pk_fma_f32 v[46:47], v[66:67], v[70:71], v[90:91] op_sel_hi:[1,0,1]
	s_nop 0
	v_pk_fma_f32 v[38:39], v[68:69], v[70:71], v[92:93] op_sel_hi:[1,0,1]
	s_nop 0
	v_pk_mul_f32 v[40:41], v[38:39], v[42:43] op_sel_hi:[1,0]
	v_pk_mul_f32 v[38:39], v[46:47], v[42:43] op_sel_hi:[1,0]
	global_store_dwordx4 v[44:45], v[38:41], off offset:64
	s_nop 1
	ds_read_b64_tr_b16 v[70:71], v164 offset:0
	ds_read_b64_tr_b16 v[72:73], v164 offset:1088
	ds_read_b128 v[66:69], v74 offset:64256
	ds_read_b64_tr_b16 v[46:47], v165 offset:0
	ds_read_b64_tr_b16 v[48:49], v165 offset:448
	ds_read_b64_tr_b16 v[42:43], v165 offset:32
	ds_read_b64_tr_b16 v[44:45], v165 offset:480
	ds_read_b64_tr_b16 v[38:39], v165 offset:64
	ds_read_b64_tr_b16 v[40:41], v165 offset:512
	ds_read_b64_tr_b16 v[214:215], v167 offset:0
	ds_read_b64_tr_b16 v[216:217], v167 offset:448
	ds_read_b64_tr_b16 v[218:219], v167 offset:32
	ds_read_b64_tr_b16 v[220:221], v167 offset:480
	ds_read_b64_tr_b16 v[222:223], v167 offset:64
	ds_read_b64_tr_b16 v[224:225], v167 offset:512
	s_waitcnt lgkmcnt(6)
	v_pk_mul_f16 v69, v69, v73
	v_pk_mul_f16 v68, v68, v72
	v_pk_mul_f16 v67, v67, v71
	v_pk_mul_f16 v66, v66, v70
	s_nop 1
	v_mfma_f32_16x16x32_f16 v[30:33], v[66:69], v[46:49], v[30:33]
	v_mfma_f32_16x16x32_f16 v[34:37], v[66:69], v[42:45], v[34:37]
	v_mfma_f32_16x16x32_f16 v[26:29], v[66:69], v[38:41], v[26:29]
	ds_read_b64_tr_b16 v[230:231], v166 offset:0
	ds_read_b64_tr_b16 v[232:233], v166 offset:1088
	ds_read_b128 v[226:229], v74 offset:64320
	ds_read_b64_tr_b16 v[46:47], v169 offset:0
	ds_read_b64_tr_b16 v[48:49], v169 offset:448
	ds_read_b64_tr_b16 v[42:43], v169 offset:32
	ds_read_b64_tr_b16 v[44:45], v169 offset:480
	ds_read_b64_tr_b16 v[38:39], v169 offset:64
	ds_read_b64_tr_b16 v[40:41], v169 offset:512
	s_waitcnt lgkmcnt(6)
	v_pk_mul_f16 v229, v229, v233
	v_pk_mul_f16 v228, v228, v232
	v_pk_mul_f16 v227, v227, v231
	v_pk_mul_f16 v226, v226, v230
	s_nop 1
	v_mfma_f32_16x16x32_f16 v[30:33], v[226:229], v[214:217], v[30:33]
	v_mfma_f32_16x16x32_f16 v[34:37], v[226:229], v[218:221], v[34:37]
	v_mfma_f32_16x16x32_f16 v[26:29], v[226:229], v[222:225], v[26:29]
	ds_read_b64_tr_b16 v[70:71], v168 offset:0
	ds_read_b64_tr_b16 v[72:73], v168 offset:1088
	ds_read_b128 v[66:69], v74 offset:64384
	ds_read_b64_tr_b16 v[214:215], v171 offset:0
	ds_read_b64_tr_b16 v[216:217], v171 offset:448
	ds_read_b64_tr_b16 v[218:219], v171 offset:32
	ds_read_b64_tr_b16 v[220:221], v171 offset:480
	ds_read_b64_tr_b16 v[222:223], v171 offset:64
	ds_read_b64_tr_b16 v[224:225], v171 offset:512
	s_waitcnt lgkmcnt(6)
	v_pk_mul_f16 v69, v69, v73
	v_pk_mul_f16 v68, v68, v72
	v_pk_mul_f16 v67, v67, v71
	v_pk_mul_f16 v66, v66, v70
	s_nop 1
	v_mfma_f32_16x16x32_f16 v[30:33], v[66:69], v[46:49], v[30:33]
	v_mfma_f32_16x16x32_f16 v[34:37], v[66:69], v[42:45], v[34:37]
	v_mfma_f32_16x16x32_f16 v[26:29], v[66:69], v[38:41], v[26:29]
	ds_read_b64_tr_b16 v[230:231], v170 offset:0
	ds_read_b64_tr_b16 v[232:233], v170 offset:1088
	ds_read_b128 v[226:229], v74 offset:64448
	s_waitcnt lgkmcnt(0)
	v_pk_mul_f16 v229, v229, v233
	v_pk_mul_f16 v228, v228, v232
	v_pk_mul_f16 v227, v227, v231
	v_pk_mul_f16 v226, v226, v230
	s_nop 1
	v_mfma_f32_16x16x32_f16 v[30:33], v[226:229], v[214:217], v[30:33]
	v_mfma_f32_16x16x32_f16 v[34:37], v[226:229], v[218:221], v[34:37]
	v_mfma_f32_16x16x32_f16 v[26:29], v[226:229], v[222:225], v[26:29]
	s_cbranch_vccnz .LBB0_3701
	ds_read_b32 v40, v135 offset:9216
	ds_read2st64_b32 v[38:39], v135 offset1:1
	s_waitcnt lgkmcnt(0)
	v_add_f32_e32 v41, v190, v40
	v_cmp_le_f32_e32 vcc, 0, v41
	s_and_saveexec_b64 s[0:1], vcc
	s_xor_b64 s[0:1], exec, s[0:1]
	s_cbranch_execz .LBB0_3795
	v_mul_f32_e32 v40, 0xbfb8aa3b, v41
	v_exp_f32_e32 v70, v40
	s_nop 0
	v_add_f32_e32 v42, 1.0, v70
	v_frexp_mant_f32_e32 v44, v42
	v_cvt_f64_f32_e32 v[40:41], v42
	v_frexp_exp_i32_f64_e32 v40, v[40:41]
	v_cmp_gt_f32_e32 vcc, s44, v44
	v_add_f32_e32 v43, -1.0, v42
	v_sub_f32_e32 v45, v43, v42
	v_subbrev_co_u32_e32 v48, vcc, 0, v40, vcc
	v_sub_u32_e32 v40, 0, v48
	v_sub_f32_e32 v43, v70, v43
	v_add_f32_e32 v45, 1.0, v45
	v_ldexp_f32 v41, v42, v40
	v_add_f32_e32 v43, v43, v45
	v_add_f32_e32 v42, -1.0, v41
	v_add_f32_e32 v44, 1.0, v41
	v_ldexp_f32 v40, v43, v40
	v_add_f32_e32 v43, 1.0, v42
	v_add_f32_e32 v45, -1.0, v44
	v_sub_f32_e32 v43, v41, v43
	v_sub_f32_e32 v41, v41, v45
	v_add_f32_e32 v43, v40, v43
	v_add_f32_e32 v40, v40, v41
	v_add_f32_e32 v49, v44, v40
	v_rcp_f32_e32 v67, v49
	v_sub_f32_e32 v41, v49, v44
	v_sub_f32_e32 v66, v40, v41
	v_add_f32_e32 v41, v42, v43
	v_mul_f32_e32 v69, v41, v67
	v_sub_f32_e32 v40, v41, v42
	v_mul_f32_e32 v42, v49, v69
	v_fma_f32 v44, v69, v49, -v42
	v_fmac_f32_e32 v44, v69, v66
	v_sub_f32_e32 v68, v43, v40
	v_add_f32_e32 v40, v42, v44
	v_sub_f32_e32 v43, v41, v40
	v_pk_add_f32 v[46:47], v[40:41], v[42:43] neg_lo:[0,1] neg_hi:[0,1]
	v_mov_b32_e32 v45, v40
	v_pk_add_f32 v[40:41], v[46:47], v[44:45] neg_lo:[0,1] neg_hi:[0,1]
	v_cmp_neq_f32_e32 vcc, s46, v70
	v_add_f32_e32 v41, v68, v41
	v_add_f32_e32 v40, v40, v41
	v_add_f32_e32 v41, v43, v40
	v_mul_f32_e32 v68, v67, v41
	v_mul_f32_e32 v42, v49, v68
	v_fma_f32 v44, v68, v49, -v42
	v_fmac_f32_e32 v44, v68, v66
	v_sub_f32_e32 v43, v43, v41
	v_add_f32_e32 v49, v40, v43
	v_add_f32_e32 v40, v42, v44
	v_sub_f32_e32 v43, v41, v40
	v_pk_add_f32 v[46:47], v[40:41], v[42:43] neg_lo:[0,1] neg_hi:[0,1]
	v_mov_b32_e32 v45, v40
	v_pk_add_f32 v[40:41], v[46:47], v[44:45] neg_lo:[0,1] neg_hi:[0,1]
	s_nop 0
	v_add_f32_e32 v41, v49, v41
	v_add_f32_e32 v40, v40, v41
	v_add_f32_e32 v41, v69, v68
	v_add_f32_e32 v40, v43, v40
	v_sub_f32_e32 v42, v41, v69
	v_mul_f32_e32 v40, v67, v40
	v_sub_f32_e32 v42, v68, v42
	v_add_f32_e32 v42, v42, v40
	v_add_f32_e32 v44, v41, v42
	v_mul_f32_e32 v45, v44, v44
	v_fmamk_f32 v40, v45, 0x3e9b6dac, v179
	v_fmaak_f32 v137, v45, v40, 0x3f2aaada
	v_cvt_f32_i32_e32 v40, v48
	v_sub_f32_e32 v41, v44, v41
	v_sub_f32_e32 v41, v42, v41
	v_ldexp_f32 v46, v41, 1
	v_mul_f32_e32 v41, v44, v45
	v_ldexp_f32 v43, v44, 1
	v_pk_mul_f32 v[44:45], v[40:41], v[136:137]
	s_nop 0
	v_fma_f32 v42, v40, s45, -v44
	v_fmac_f32_e32 v42, 0xb102e308, v40
	v_pk_add_f32 v[40:41], v[44:45], v[42:43]
	s_nop 0
	v_sub_f32_e32 v43, v41, v43
	v_sub_f32_e32 v43, v45, v43
	v_add_f32_e32 v47, v46, v43
	v_mov_b32_e32 v46, v44
	v_pk_add_f32 v[44:45], v[40:41], v[44:45] neg_lo:[0,1] neg_hi:[0,1]
	v_pk_add_f32 v[48:49], v[40:41], v[46:47]
	v_mov_b32_e32 v43, v40
	v_mov_b32_e32 v45, v49
	v_pk_add_f32 v[66:67], v[42:43], v[44:45] neg_lo:[0,1] neg_hi:[0,1]
	v_pk_add_f32 v[42:43], v[42:43], v[44:45]
	v_mov_b32_e32 v46, v47
	v_pk_add_f32 v[44:45], v[42:43], v[40:41] op_sel:[1,0] op_sel_hi:[0,1] neg_lo:[0,1] neg_hi:[0,1]
	v_pk_add_f32 v[68:69], v[48:49], v[44:45] op_sel_hi:[1,0] neg_lo:[0,1] neg_hi:[0,1]
	v_mov_b32_e32 v48, v49
	v_mov_b32_e32 v49, v43
	v_pk_mov_b32 v[44:45], v[40:41], v[44:45] op_sel:[1,0]
	v_mov_b32_e32 v47, v40
	v_pk_add_f32 v[44:45], v[48:49], v[44:45] neg_lo:[0,1] neg_hi:[0,1]
	v_mov_b32_e32 v68, v66
	v_pk_add_f32 v[40:41], v[46:47], v[44:45] neg_lo:[0,1] neg_hi:[0,1]
	v_mov_b32_e32 v67, v43
	v_pk_add_f32 v[44:45], v[68:69], v[40:41]
	s_nop 0
	v_pk_add_f32 v[46:47], v[44:45], v[44:45] op_sel:[0,1] op_sel_hi:[1,0]
	s_nop 0
	v_pk_add_f32 v[42:43], v[42:43], v[46:47] op_sel:[1,0] op_sel_hi:[0,1]
	v_mov_b32_e32 v45, v42
	v_pk_add_f32 v[48:49], v[44:45], v[66:67] neg_lo:[0,1] neg_hi:[0,1]
	v_mov_b32_e32 v41, v46
	v_sub_f32_e32 v43, v44, v48
	v_pk_add_f32 v[40:41], v[40:41], v[48:49] neg_lo:[0,1] neg_hi:[0,1]
	v_sub_f32_e32 v43, v66, v43
	v_add_f32_e32 v40, v40, v43
	v_add_f32_e32 v40, v40, v41
	v_add_f32_e32 v40, v42, v40
	v_cndmask_b32_e32 v40, v183, v40, vcc
	v_cmp_ngt_f32_e32 vcc, -1.0, v70
	s_nop 1
	v_cndmask_b32_e32 v40, v184, v40, vcc
	v_cmp_neq_f32_e32 vcc, -1.0, v70
	s_nop 1
	v_cndmask_b32_e32 v40, v185, v40, vcc
	v_cmp_lt_f32_e64 vcc, |v70|, s47
	s_nop 1
	v_cndmask_b32_e32 v40, v40, v70, vcc
	v_xor_b32_e32 v40, 0x80000000, v40

.LBB0_5080:
	s_add_i32 s52, s47, -1
	s_bitcmp1_b32 s52, 0
	s_cselect_b32 s2, 0xa00, 0
	s_add_i32 s81, s2, 0
	v_mov_b32_e32 v70, s81
	ds_read_b32 v146, v70 offset:64512
	v_cndmask_b32_e64 v70, 0, 1, s[82:83]
	v_mov_b32_e32 v72, 0
	v_cmp_ne_u32_e64 s[86:87], 1, v70
	s_andn2_b64 vcc, exec, s[82:83]
	v_mov_b32_e32 v100, 0
	v_mov_b32_e32 v101, 0
	v_mov_b32_e32 v102, 0
	v_mov_b32_e32 v103, 0
	s_cbranch_vccnz .LBB0_5082
	ds_read_b128 v[74:77], v187
	ds_read_b128 v[78:81], v187 offset:64
	ds_read_b128 v[202:205], v187 offset:128
	ds_read_b128 v[206:209], v187 offset:192
	s_waitcnt lgkmcnt(3)
	v_mfma_f32_16x16x32_f16 v[74:77], v[74:77], v[66:69], 0
	s_waitcnt lgkmcnt(2)
	v_mfma_f32_16x16x32_f16 v[74:77], v[78:81], v[46:49], v[74:77]
	s_waitcnt lgkmcnt(1)
	v_mfma_f32_16x16x32_f16 v[74:77], v[202:205], v[42:45], v[74:77]
	s_waitcnt lgkmcnt(0)
	v_mfma_f32_16x16x32_f16 v[100:103], v[206:209], v[38:41], v[74:77]
.LBB0_5082:
	v_cndmask_b32_e64 v70, 0, 1, s[12:13]
	v_cmp_ne_u32_e64 s[78:79], 1, v70
	s_andn2_b64 vcc, exec, s[12:13]
	v_mov_b32_e32 v73, 0
	s_nop 0
	v_mov_b32_e32 v74, 0
	v_mov_b32_e32 v75, 0
	s_cbranch_vccnz .LBB0_5084
	ds_read_b128 v[70:73], v187 offset:4352
	ds_read_b128 v[74:77], v187 offset:4416
	ds_read_b128 v[202:205], v187 offset:4480
	ds_read_b128 v[206:209], v187 offset:4544
	s_waitcnt lgkmcnt(3)
	v_mfma_f32_16x16x32_f16 v[70:73], v[70:73], v[66:69], 0
	s_waitcnt lgkmcnt(2)
	v_mfma_f32_16x16x32_f16 v[70:73], v[74:77], v[46:49], v[70:73]
	s_waitcnt lgkmcnt(1)
	v_mfma_f32_16x16x32_f16 v[70:73], v[202:205], v[42:45], v[70:73]
	s_waitcnt lgkmcnt(0)
	v_mfma_f32_16x16x32_f16 v[72:75], v[206:209], v[38:41], v[70:73]
.LBB0_5084:
	s_nop 4
	v_cndmask_b32_e64 v70, 0, 1, s[14:15]
	v_mov_b32_e32 v76, 0
	v_cmp_ne_u32_e64 s[88:89], 1, v70
	s_andn2_b64 vcc, exec, s[14:15]
	v_mov_b32_e32 v96, 0
	v_mov_b32_e32 v97, 0
	v_mov_b32_e32 v98, 0
	v_mov_b32_e32 v99, 0
	s_cbranch_vccnz .LBB0_5086
	ds_read_b128 v[78:81], v187 offset:8704
	ds_read_b128 v[82:85], v187 offset:8768
	ds_read_b128 v[202:205], v187 offset:8832
	ds_read_b128 v[206:209], v187 offset:8896
	s_waitcnt lgkmcnt(3)
	v_mfma_f32_16x16x32_f16 v[78:81], v[78:81], v[66:69], 0
	s_waitcnt lgkmcnt(2)
	v_mfma_f32_16x16x32_f16 v[78:81], v[82:85], v[46:49], v[78:81]
	s_waitcnt lgkmcnt(1)
	v_mfma_f32_16x16x32_f16 v[78:81], v[202:205], v[42:45], v[78:81]
	s_waitcnt lgkmcnt(0)
	v_mfma_f32_16x16x32_f16 v[96:99], v[206:209], v[38:41], v[78:81]
.LBB0_5086:
	v_cndmask_b32_e64 v70, 0, 1, s[16:17]
	v_cmp_ne_u32_e64 s[2:3], 1, v70
	s_andn2_b64 vcc, exec, s[16:17]
	v_mov_b32_e32 v77, 0
	s_nop 0
	v_mov_b32_e32 v78, 0
	v_mov_b32_e32 v79, 0
	s_cbranch_vccnz .LBB0_5088
	ds_read_b128 v[76:79], v187 offset:13056
	ds_read_b128 v[80:83], v187 offset:13120
	ds_read_b128 v[202:205], v187 offset:13184
	ds_read_b128 v[206:209], v187 offset:13248
	s_waitcnt lgkmcnt(3)
	v_mfma_f32_16x16x32_f16 v[76:79], v[76:79], v[66:69], 0
	s_waitcnt lgkmcnt(2)
	v_mfma_f32_16x16x32_f16 v[76:79], v[80:83], v[46:49], v[76:79]
	s_waitcnt lgkmcnt(1)
	v_mfma_f32_16x16x32_f16 v[76:79], v[202:205], v[42:45], v[76:79]
	s_waitcnt lgkmcnt(0)
	v_mfma_f32_16x16x32_f16 v[76:79], v[206:209], v[38:41], v[76:79]
.LBB0_5088:
	v_cndmask_b32_e64 v70, 0, 1, s[18:19]
	v_mov_b32_e32 v80, 0
	v_cmp_ne_u32_e64 s[90:91], 1, v70
	s_andn2_b64 vcc, exec, s[18:19]
	v_mov_b32_e32 v92, 0
	v_mov_b32_e32 v93, 0
	v_mov_b32_e32 v94, 0
	v_mov_b32_e32 v95, 0
	s_cbranch_vccnz .LBB0_5090
	ds_read_b128 v[82:85], v187 offset:17408
	ds_read_b128 v[86:89], v187 offset:17472
	ds_read_b128 v[202:205], v187 offset:17536
	ds_read_b128 v[206:209], v187 offset:17600
	s_waitcnt lgkmcnt(3)
	v_mfma_f32_16x16x32_f16 v[82:85], v[82:85], v[66:69], 0
	s_waitcnt lgkmcnt(2)
	v_mfma_f32_16x16x32_f16 v[82:85], v[86:89], v[46:49], v[82:85]
	s_waitcnt lgkmcnt(1)
	v_mfma_f32_16x16x32_f16 v[82:85], v[202:205], v[42:45], v[82:85]
	s_waitcnt lgkmcnt(0)
	v_mfma_f32_16x16x32_f16 v[92:95], v[206:209], v[38:41], v[82:85]
.LBB0_5090:
	v_cndmask_b32_e64 v70, 0, 1, s[20:21]
	v_cmp_ne_u32_e64 s[96:97], 1, v70
	s_andn2_b64 vcc, exec, s[20:21]
	v_mov_b32_e32 v81, 0
	s_nop 0
	v_mov_b32_e32 v82, 0
	v_mov_b32_e32 v83, 0
	s_cbranch_vccnz .LBB0_5092
	ds_read_b128 v[80:83], v187 offset:21760
	ds_read_b128 v[84:87], v187 offset:21824
	ds_read_b128 v[202:205], v187 offset:21888
	ds_read_b128 v[206:209], v187 offset:21952
	s_waitcnt lgkmcnt(3)
	v_mfma_f32_16x16x32_f16 v[80:83], v[80:83], v[66:69], 0
	s_waitcnt lgkmcnt(2)
	v_mfma_f32_16x16x32_f16 v[80:83], v[84:87], v[46:49], v[80:83]
	s_waitcnt lgkmcnt(1)
	v_mfma_f32_16x16x32_f16 v[80:83], v[202:205], v[42:45], v[80:83]
	s_waitcnt lgkmcnt(0)
	v_mfma_f32_16x16x32_f16 v[80:83], v[206:209], v[38:41], v[80:83]
.LBB0_5092:
	v_cndmask_b32_e64 v70, 0, 1, s[22:23]
	v_mov_b32_e32 v84, 0
	v_cmp_ne_u32_e64 s[92:93], 1, v70
	s_andn2_b64 vcc, exec, s[22:23]
	v_mov_b32_e32 v88, 0
	v_mov_b32_e32 v89, 0
	v_mov_b32_e32 v90, 0
	v_mov_b32_e32 v91, 0
	s_cbranch_vccnz .LBB0_5094
	ds_read_b128 v[86:89], v187 offset:26112
	ds_read_b128 v[192:195], v187 offset:26176
	ds_read_b128 v[202:205], v187 offset:26240
	ds_read_b128 v[206:209], v187 offset:26304
	s_waitcnt lgkmcnt(3)
	v_mfma_f32_16x16x32_f16 v[86:89], v[86:89], v[66:69], 0
	s_waitcnt lgkmcnt(2)
	v_mfma_f32_16x16x32_f16 v[86:89], v[192:195], v[46:49], v[86:89]
	s_waitcnt lgkmcnt(1)
	v_mfma_f32_16x16x32_f16 v[86:89], v[202:205], v[42:45], v[86:89]
	s_waitcnt lgkmcnt(0)
	v_mfma_f32_16x16x32_f16 v[88:91], v[206:209], v[38:41], v[86:89]
.LBB0_5094:
	v_cndmask_b32_e64 v70, 0, 1, s[24:25]
	v_cmp_ne_u32_e64 s[94:95], 1, v70
	s_andn2_b64 vcc, exec, s[24:25]
	v_mov_b32_e32 v85, 0
	s_nop 0
	v_mov_b32_e32 v86, 0
	v_mov_b32_e32 v87, 0
	s_cbranch_vccnz .LBB0_5096
	ds_read_b128 v[84:87], v187 offset:30464
	ds_read_b128 v[192:195], v187 offset:30528
	ds_read_b128 v[202:205], v187 offset:30592
	ds_read_b128 v[206:209], v187 offset:30656
	s_waitcnt lgkmcnt(3)
	v_mfma_f32_16x16x32_f16 v[84:87], v[84:87], v[66:69], 0
	s_waitcnt lgkmcnt(2)
	v_mfma_f32_16x16x32_f16 v[84:87], v[192:195], v[46:49], v[84:87]
	s_waitcnt lgkmcnt(1)
	v_mfma_f32_16x16x32_f16 v[84:87], v[202:205], v[42:45], v[84:87]
	s_waitcnt lgkmcnt(0)
	v_mfma_f32_16x16x32_f16 v[84:87], v[206:209], v[38:41], v[84:87]

.LBB0_5155:
	ds_read_b128 v[74:77], v187 offset:49152
	ds_read_b128 v[78:81], v187 offset:53504
	ds_read_b128 v[82:85], v187 offset:57856
	ds_read_b128 v[202:205], v187 offset:49216
	ds_read_b128 v[206:209], v187 offset:53568
	ds_read_b128 v[214:217], v187 offset:57920
	ds_read_b128 v[218:221], v187 offset:49280
	ds_read_b128 v[222:225], v187 offset:53632
	ds_read_b128 v[226:229], v187 offset:57984
	ds_read_b128 v[230:233], v187 offset:49344
	ds_read_b128 v[234:237], v187 offset:53696
	ds_read_b128 v[238:241], v187 offset:58048
	s_cmp_lt_u32 s52, 2
	s_cselect_b64 vcc, -1, 0
	s_and_b64 s[2:3], vcc, exec
	s_movk_i32 s2, 0x7ff
	s_nop 0
	v_cndmask_b32_e32 v71, v153, v147, vcc
	s_cselect_b32 s2, 0xff, s2
	s_waitcnt lgkmcnt(11)
	v_mfma_f32_16x16x32_f16 v[74:77], v[74:77], v[66:69], 0
	v_add_u32_e32 v73, s48, v71
	v_sub_u32_e32 v71, s2, v71
	v_mov_b32_e32 v72, s46
	s_waitcnt lgkmcnt(10)
	v_mfma_f32_16x16x32_f16 v[78:81], v[78:81], v[66:69], 0
	v_cndmask_b32_e32 v72, v72, v191, vcc
	v_add_u32_e32 v71, s49, v71
	v_add_u32_e32 v71, 0x80, v71
	s_waitcnt lgkmcnt(9)
	v_mfma_f32_16x16x32_f16 v[66:69], v[82:85], v[66:69], 0
	v_cndmask_b32_e64 v71, v71, v73, s[84:85]
	v_add_u32_e32 v72, v71, v72
	s_waitcnt lgkmcnt(8)
	v_mfma_f32_16x16x32_f16 v[74:77], v[202:205], v[46:49], v[74:77]
	v_ashrrev_i32_e32 v73, 31, v72
	v_pk_mul_f32 v[32:33], v[32:33], v[146:147] op_sel_hi:[1,0]
	s_waitcnt lgkmcnt(7)
	v_mfma_f32_16x16x32_f16 v[78:81], v[206:209], v[46:49], v[78:81]
	v_pk_mul_f32 v[30:31], v[30:31], v[146:147] op_sel_hi:[1,0]
	v_pk_mul_f32 v[36:37], v[36:37], v[146:147] op_sel_hi:[1,0]
	s_waitcnt lgkmcnt(6)
	v_mfma_f32_16x16x32_f16 v[46:49], v[214:217], v[46:49], v[66:69]
	v_pk_mul_f32 v[34:35], v[34:35], v[146:147] op_sel_hi:[1,0]
	v_pk_mul_f32 v[28:29], v[28:29], v[146:147] op_sel_hi:[1,0]
	s_waitcnt lgkmcnt(5)
	v_mfma_f32_16x16x32_f16 v[66:69], v[218:221], v[42:45], v[74:77]
	v_pk_mul_f32 v[26:27], v[26:27], v[146:147] op_sel_hi:[1,0]
	s_waitcnt lgkmcnt(4)
	v_mfma_f32_16x16x32_f16 v[74:77], v[222:225], v[42:45], v[78:81]
	s_waitcnt lgkmcnt(3)
	v_mfma_f32_16x16x32_f16 v[42:45], v[226:229], v[42:45], v[46:49]
	s_waitcnt lgkmcnt(2)
	v_mfma_f32_16x16x32_f16 v[46:49], v[230:233], v[38:41], v[66:69]
	s_waitcnt lgkmcnt(1)
	v_mfma_f32_16x16x32_f16 v[66:69], v[234:237], v[38:41], v[74:77]
	s_waitcnt lgkmcnt(0)
	v_mfma_f32_16x16x32_f16 v[38:41], v[238:241], v[38:41], v[42:45]
	v_lshl_add_u32 v74, v112, 1, s81
	s_nop 6
	ds_read2st64_b32 v[40:41], v137 offset0:247 offset1:249
	s_waitcnt lgkmcnt(0)
	v_fmac_f32_e32 v70, v41, v38
	v_and_or_b32 v38, v180, 64, v113
	v_lshlrev_b32_e32 v38, 2, v38
	ds_bpermute_b32 v38, v38, v70
	v_max_f32_e32 v39, v40, v40
	v_mov_b32_e32 v70, v41
	v_pk_fma_f32 v[46:47], v[46:47], v[70:71], v[86:87] op_sel_hi:[1,0,1]
	s_waitcnt lgkmcnt(0)
	v_max_f32_e64 v38, |v38|, |v38|
	v_max_f32_e32 v38, v38, v39
	v_div_scale_f32 v39, s[2:3], v38, v38, 1.0
	v_rcp_f32_e32 v40, v39
	s_or_b64 s[2:3], s[4:5], s[34:35]
	v_fma_f32 v42, -v39, v40, 1.0
	v_fmac_f32_e32 v40, v42, v40
	v_div_scale_f32 v42, vcc, 1.0, v38, 1.0
	v_mul_f32_e32 v43, v42, v40
	v_fma_f32 v44, -v39, v43, v42
	v_fmac_f32_e32 v43, v44, v40
	v_fma_f32 v39, -v39, v43, v42
	v_div_fmas_f32 v39, v39, v40, v43
	v_div_fixup_f32 v42, v39, v38, 1.0
	v_lshl_add_u64 v[38:39], v[72:73], 0, s[28:29]
	v_lshlrev_b64 v[38:39], 11, v[38:39]
	v_lshl_add_u64 v[44:45], v[142:143], 0, v[38:39]
	v_pk_fma_f32 v[38:39], v[48:49], v[70:71], v[88:89] op_sel_hi:[1,0,1]
	s_and_b64 vcc, exec, s[2:3]
	v_pk_mul_f32 v[40:41], v[38:39], v[42:43] op_sel_hi:[1,0]
	v_pk_mul_f32 v[38:39], v[46:47], v[42:43] op_sel_hi:[1,0]
	global_store_dwordx4 v[44:45], v[38:41], off
	v_pk_fma_f32 v[46:47], v[66:67], v[70:71], v[90:91] op_sel_hi:[1,0,1]
	s_nop 0
	v_pk_fma_f32 v[38:39], v[68:69], v[70:71], v[92:93] op_sel_hi:[1,0,1]
	s_nop 0
	v_pk_mul_f32 v[40:41], v[38:39], v[42:43] op_sel_hi:[1,0]
	v_pk_mul_f32 v[38:39], v[46:47], v[42:43] op_sel_hi:[1,0]
	global_store_dwordx4 v[44:45], v[38:41], off offset:64
	s_nop 1
	ds_read_b64_tr_b16 v[70:71], v164 offset:0
	ds_read_b64_tr_b16 v[72:73], v164 offset:1088
	ds_read_b128 v[66:69], v74 offset:64256
	ds_read_b64_tr_b16 v[46:47], v165 offset:0
	ds_read_b64_tr_b16 v[48:49], v165 offset:448
	ds_read_b64_tr_b16 v[42:43], v165 offset:32
	ds_read_b64_tr_b16 v[44:45], v165 offset:480
	ds_read_b64_tr_b16 v[38:39], v165 offset:64
	ds_read_b64_tr_b16 v[40:41], v165 offset:512
	ds_read_b64_tr_b16 v[214:215], v167 offset:0
	ds_read_b64_tr_b16 v[216:217], v167 offset:448
	ds_read_b64_tr_b16 v[218:219], v167 offset:32
	ds_read_b64_tr_b16 v[220:221], v167 offset:480
	ds_read_b64_tr_b16 v[222:223], v167 offset:64
	ds_read_b64_tr_b16 v[224:225], v167 offset:512
	s_waitcnt lgkmcnt(6)
	v_pk_mul_f16 v69, v69, v73
	v_pk_mul_f16 v68, v68, v72
	v_pk_mul_f16 v67, v67, v71
	v_pk_mul_f16 v66, v66, v70
	s_nop 1
	v_mfma_f32_16x16x32_f16 v[30:33], v[66:69], v[46:49], v[30:33]
	v_mfma_f32_16x16x32_f16 v[34:37], v[66:69], v[42:45], v[34:37]
	v_mfma_f32_16x16x32_f16 v[26:29], v[66:69], v[38:41], v[26:29]
	ds_read_b64_tr_b16 v[230:231], v166 offset:0
	ds_read_b64_tr_b16 v[232:233], v166 offset:1088
	ds_read_b128 v[226:229], v74 offset:64320
	ds_read_b64_tr_b16 v[46:47], v169 offset:0
	ds_read_b64_tr_b16 v[48:49], v169 offset:448
	ds_read_b64_tr_b16 v[42:43], v169 offset:32
	ds_read_b64_tr_b16 v[44:45], v169 offset:480
	ds_read_b64_tr_b16 v[38:39], v169 offset:64
	ds_read_b64_tr_b16 v[40:41], v169 offset:512
	s_waitcnt lgkmcnt(6)
	v_pk_mul_f16 v229, v229, v233
	v_pk_mul_f16 v228, v228, v232
	v_pk_mul_f16 v227, v227, v231
	v_pk_mul_f16 v226, v226, v230
	s_nop 1
	v_mfma_f32_16x16x32_f16 v[30:33], v[226:229], v[214:217], v[30:33]
	v_mfma_f32_16x16x32_f16 v[34:37], v[226:229], v[218:221], v[34:37]
	v_mfma_f32_16x16x32_f16 v[26:29], v[226:229], v[222:225], v[26:29]
	ds_read_b64_tr_b16 v[70:71], v168 offset:0
	ds_read_b64_tr_b16 v[72:73], v168 offset:1088
	ds_read_b128 v[66:69], v74 offset:64384
	ds_read_b64_tr_b16 v[214:215], v171 offset:0
	ds_read_b64_tr_b16 v[216:217], v171 offset:448
	ds_read_b64_tr_b16 v[218:219], v171 offset:32
	ds_read_b64_tr_b16 v[220:221], v171 offset:480
	ds_read_b64_tr_b16 v[222:223], v171 offset:64
	ds_read_b64_tr_b16 v[224:225], v171 offset:512
	s_waitcnt lgkmcnt(6)
	v_pk_mul_f16 v69, v69, v73
	v_pk_mul_f16 v68, v68, v72
	v_pk_mul_f16 v67, v67, v71
	v_pk_mul_f16 v66, v66, v70
	s_nop 1
	v_mfma_f32_16x16x32_f16 v[30:33], v[66:69], v[46:49], v[30:33]
	v_mfma_f32_16x16x32_f16 v[34:37], v[66:69], v[42:45], v[34:37]
	v_mfma_f32_16x16x32_f16 v[26:29], v[66:69], v[38:41], v[26:29]
	ds_read_b64_tr_b16 v[230:231], v170 offset:0
	ds_read_b64_tr_b16 v[232:233], v170 offset:1088
	ds_read_b128 v[226:229], v74 offset:64448
	s_waitcnt lgkmcnt(0)
	v_pk_mul_f16 v229, v229, v233
	v_pk_mul_f16 v228, v228, v232
	v_pk_mul_f16 v227, v227, v231
	v_pk_mul_f16 v226, v226, v230
	s_nop 1
	v_mfma_f32_16x16x32_f16 v[30:33], v[226:229], v[214:217], v[30:33]
	v_mfma_f32_16x16x32_f16 v[34:37], v[226:229], v[218:221], v[34:37]
	v_mfma_f32_16x16x32_f16 v[26:29], v[226:229], v[222:225], v[26:29]
	s_cbranch_vccnz .LBB0_5064
	ds_read_b32 v40, v135 offset:9216
	ds_read2st64_b32 v[38:39], v135 offset1:1
	s_waitcnt lgkmcnt(0)
	v_add_f32_e32 v41, v190, v40
	v_cmp_le_f32_e32 vcc, 0, v41
	s_and_saveexec_b64 s[2:3], vcc
	s_xor_b64 s[2:3], exec, s[2:3]
	s_cbranch_execz .LBB0_5158
	v_mul_f32_e32 v40, 0xbfb8aa3b, v41
	v_exp_f32_e32 v70, v40
	s_nop 0
	v_add_f32_e32 v42, 1.0, v70
	v_frexp_mant_f32_e32 v44, v42
	v_cvt_f64_f32_e32 v[40:41], v42
	v_frexp_exp_i32_f64_e32 v40, v[40:41]
	v_cmp_gt_f32_e32 vcc, s42, v44
	v_add_f32_e32 v43, -1.0, v42
	v_sub_f32_e32 v45, v43, v42
	v_subbrev_co_u32_e32 v48, vcc, 0, v40, vcc
	v_sub_u32_e32 v40, 0, v48
	v_sub_f32_e32 v43, v70, v43
	v_add_f32_e32 v45, 1.0, v45
	v_ldexp_f32 v41, v42, v40
	v_add_f32_e32 v43, v43, v45
	v_add_f32_e32 v42, -1.0, v41
	v_add_f32_e32 v44, 1.0, v41
	v_ldexp_f32 v40, v43, v40
	v_add_f32_e32 v43, 1.0, v42
	v_add_f32_e32 v45, -1.0, v44
	v_sub_f32_e32 v43, v41, v43
	v_sub_f32_e32 v41, v41, v45
	v_add_f32_e32 v43, v40, v43
	v_add_f32_e32 v40, v40, v41
	v_add_f32_e32 v49, v44, v40
	v_rcp_f32_e32 v67, v49
	v_sub_f32_e32 v41, v49, v44
	v_sub_f32_e32 v66, v40, v41
	v_add_f32_e32 v41, v42, v43
	v_mul_f32_e32 v69, v41, v67
	v_sub_f32_e32 v40, v41, v42
	v_mul_f32_e32 v42, v49, v69
	v_fma_f32 v44, v69, v49, -v42
	v_fmac_f32_e32 v44, v69, v66
	v_sub_f32_e32 v68, v43, v40
	v_add_f32_e32 v40, v42, v44
	v_sub_f32_e32 v43, v41, v40
	v_pk_add_f32 v[46:47], v[40:41], v[42:43] neg_lo:[0,1] neg_hi:[0,1]
	v_mov_b32_e32 v45, v40
	v_pk_add_f32 v[40:41], v[46:47], v[44:45] neg_lo:[0,1] neg_hi:[0,1]
	v_cmp_neq_f32_e32 vcc, s44, v70
	v_add_f32_e32 v41, v68, v41
	v_add_f32_e32 v40, v40, v41
	v_add_f32_e32 v41, v43, v40
	v_mul_f32_e32 v68, v67, v41
	v_mul_f32_e32 v42, v49, v68
	v_fma_f32 v44, v68, v49, -v42
	v_fmac_f32_e32 v44, v68, v66
	v_sub_f32_e32 v43, v43, v41
	v_add_f32_e32 v49, v40, v43
	v_add_f32_e32 v40, v42, v44
	v_sub_f32_e32 v43, v41, v40
	v_pk_add_f32 v[46:47], v[40:41], v[42:43] neg_lo:[0,1] neg_hi:[0,1]
	v_mov_b32_e32 v45, v40
	v_pk_add_f32 v[40:41], v[46:47], v[44:45] neg_lo:[0,1] neg_hi:[0,1]
	s_nop 0
	v_add_f32_e32 v41, v49, v41
	v_add_f32_e32 v40, v40, v41
	v_add_f32_e32 v41, v69, v68
	v_add_f32_e32 v40, v43, v40
	v_sub_f32_e32 v42, v41, v69
	v_mul_f32_e32 v40, v67, v40
	v_sub_f32_e32 v42, v68, v42
	v_add_f32_e32 v42, v42, v40
	v_add_f32_e32 v44, v41, v42
	v_mul_f32_e32 v45, v44, v44
	v_fmamk_f32 v40, v45, 0x3e9b6dac, v179
	v_fmaak_f32 v137, v45, v40, 0x3f2aaada
	v_cvt_f32_i32_e32 v40, v48
	v_sub_f32_e32 v41, v44, v41
	v_sub_f32_e32 v41, v42, v41
	v_ldexp_f32 v46, v41, 1
	v_mul_f32_e32 v41, v44, v45
	v_ldexp_f32 v43, v44, 1
	v_pk_mul_f32 v[44:45], v[40:41], v[136:137]
	s_nop 0
	v_fma_f32 v42, v40, s43, -v44
	v_fmac_f32_e32 v42, 0xb102e308, v40
	v_pk_add_f32 v[40:41], v[44:45], v[42:43]
	s_nop 0
	v_sub_f32_e32 v43, v41, v43
	v_sub_f32_e32 v43, v45, v43
	v_add_f32_e32 v47, v46, v43
	v_mov_b32_e32 v46, v44
	v_pk_add_f32 v[44:45], v[40:41], v[44:45] neg_lo:[0,1] neg_hi:[0,1]
	v_pk_add_f32 v[48:49], v[40:41], v[46:47]
	v_mov_b32_e32 v43, v40
	v_mov_b32_e32 v45, v49
	v_pk_add_f32 v[66:67], v[42:43], v[44:45] neg_lo:[0,1] neg_hi:[0,1]
	v_pk_add_f32 v[42:43], v[42:43], v[44:45]
	v_mov_b32_e32 v46, v47
	v_pk_add_f32 v[44:45], v[42:43], v[40:41] op_sel:[1,0] op_sel_hi:[0,1] neg_lo:[0,1] neg_hi:[0,1]
	v_pk_add_f32 v[68:69], v[48:49], v[44:45] op_sel_hi:[1,0] neg_lo:[0,1] neg_hi:[0,1]
	v_mov_b32_e32 v48, v49
	v_mov_b32_e32 v49, v43
	v_pk_mov_b32 v[44:45], v[40:41], v[44:45] op_sel:[1,0]
	v_mov_b32_e32 v47, v40
	v_pk_add_f32 v[44:45], v[48:49], v[44:45] neg_lo:[0,1] neg_hi:[0,1]
	v_mov_b32_e32 v68, v66
	v_pk_add_f32 v[40:41], v[46:47], v[44:45] neg_lo:[0,1] neg_hi:[0,1]
	v_mov_b32_e32 v67, v43
	v_pk_add_f32 v[44:45], v[68:69], v[40:41]
	s_nop 0
	v_pk_add_f32 v[46:47], v[44:45], v[44:45] op_sel:[0,1] op_sel_hi:[1,0]
	s_nop 0
	v_pk_add_f32 v[42:43], v[42:43], v[46:47] op_sel:[1,0] op_sel_hi:[0,1]
	v_mov_b32_e32 v45, v42
	v_pk_add_f32 v[48:49], v[44:45], v[66:67] neg_lo:[0,1] neg_hi:[0,1]
	v_mov_b32_e32 v41, v46
	v_sub_f32_e32 v43, v44, v48
	v_pk_add_f32 v[40:41], v[40:41], v[48:49] neg_lo:[0,1] neg_hi:[0,1]
	v_sub_f32_e32 v43, v66, v43
	v_add_f32_e32 v40, v40, v43
	v_add_f32_e32 v40, v40, v41
	v_add_f32_e32 v40, v42, v40
	v_cndmask_b32_e32 v40, v183, v40, vcc
	v_cmp_ngt_f32_e32 vcc, -1.0, v70
	s_nop 1
	v_cndmask_b32_e32 v40, v184, v40, vcc
	v_cmp_neq_f32_e32 vcc, -1.0, v70
	s_nop 1
	v_cndmask_b32_e32 v40, v185, v40, vcc
	v_cmp_lt_f32_e64 vcc, |v70|, s45
	s_nop 1
	v_cndmask_b32_e32 v40, v40, v70, vcc
	v_xor_b32_e32 v40, 0x80000000, v40
